# combo3 = combo2 + attention Q fragments fetched one tile ahead + hmpost token loop unrolled with loads issued up front
# speedup vs baseline: 1.0180x; 1.0180x over previous
.LBB0_615:
	s_cmp_lt_i32 s48, 5
	s_cselect_b64 s[6:7], -1, 0
	s_and_b64 s[10:11], s[6:7], s[4:5]
	s_andn2_b64 vcc, exec, s[10:11]
	s_cbranch_vccnz .LBB0_620
	v_lshrrev_b32_e32 v1, 6, v0
	s_waitcnt vmcnt(3)
	v_lshl_or_b32 v18, s2, 3, v1
	s_movk_i32 s4, 0x4000
	v_cmp_gt_i32_e32 vcc, s4, v18
	s_and_saveexec_b64 s[12:13], vcc
	s_cbranch_execz .LBB0_619
	s_load_dwordx2 s[4:5], s[0:1], 0x30
	v_lshlrev_b32_e32 v1, 4, v0
	v_and_b32_e32 v1, 0x3f0, v1
	s_lshl_b32 s14, s3, 3
	s_movk_i32 s6, 0x4c00
	s_waitcnt lgkmcnt(0)
	global_load_dwordx4 v[2:5], v1, s[4:5] offset:3072
	global_load_dwordx4 v[6:9], v1, s[4:5] offset:2048
	global_load_dwordx4 v[10:13], v1, s[4:5] offset:1024
	global_load_dwordx4 v[14:17], v1, s[4:5]
	v_mbcnt_lo_u32_b32 v1, -1, 0
	v_mbcnt_hi_u32_b32 v19, -1, v1
	v_and_b32_e32 v1, 64, v19
	v_add_u32_e32 v20, 64, v1
	v_xor_b32_e32 v1, 32, v19
	v_cmp_lt_i32_e32 vcc, v1, v20
	v_xor_b32_e32 v21, 16, v19
	s_load_dwordx2 s[4:5], s[0:1], 0xb0
	v_cndmask_b32_e32 v1, v19, v1, vcc
	v_cmp_lt_i32_e32 vcc, v21, v20
	s_ashr_i32 s15, s14, 31
	v_lshlrev_b32_e32 v1, 2, v1
	v_cndmask_b32_e32 v21, v19, v21, vcc
	v_lshlrev_b32_e32 v34, 2, v21
	v_xor_b32_e32 v21, 8, v19
	v_cmp_lt_i32_e32 vcc, v21, v20
	s_waitcnt vmcnt(6) lgkmcnt(0)
	v_mov_b64_e32 v[22:23], s[4:5]
	v_mad_i64_i32 v[22:23], s[6:7], v18, s6, v[22:23]
	v_cndmask_b32_e32 v21, v19, v21, vcc
	v_lshlrev_b32_e32 v35, 2, v21
	v_xor_b32_e32 v21, 4, v19
	v_cmp_lt_i32_e32 vcc, v21, v20
	s_mul_i32 s16, s3, 0x26000
	s_mul_hi_i32 s17, s14, 0x4c00
	v_cndmask_b32_e32 v21, v19, v21, vcc
	v_lshlrev_b32_e32 v36, 2, v21
	v_xor_b32_e32 v21, 2, v19
	v_cmp_lt_i32_e32 vcc, v21, v20
	s_lshl_b64 s[18:19], s[14:15], 11
	s_mov_b64 s[20:21], 0
	v_cndmask_b32_e32 v21, v19, v21, vcc
	v_lshlrev_b32_e32 v37, 2, v21
	v_xor_b32_e32 v21, 1, v19
	v_cmp_lt_i32_e32 vcc, v21, v20
	s_mov_b32 s22, 0x3b800000
	s_mov_b32 s15, 0x800000
	v_cndmask_b32_e32 v19, v19, v21, vcc
	v_lshlrev_b32_e32 v38, 2, v19
	v_and_b32_e32 v19, 63, v0
	v_lshlrev_b32_e32 v20, 3, v19
	v_ashrrev_i32_e32 v19, 31, v18
	v_lshlrev_b64 v[24:25], 11, v[18:19]
	v_lshl_add_u64 v[24:25], s[4:5], 0, v[24:25]
	s_mov_b32 s4, 0x358637bd
	v_mov_b32_e32 v21, 0
	s_mov_b32 s23, 0x2b80a000
	s_movk_i32 s24, 0x3fff
	s_waitcnt vmcnt(5)
	v_mov_b64_e32 v[26:27], s[4:5]
	v_lshl_add_u64 v[228:229], v[24:25], 0, v[20:21]
	v_lshl_add_u64 v[230:231], v[22:23], 0, v[20:21]
	v_add_co_u32_e32 v228, vcc, 0x3ec4a000, v228
	s_nop 1
	v_addc_co_u32_e32 v229, vcc, 0, v229, vcc
	v_add_co_u32_e32 v230, vcc, 0x42c4b000, v230
	s_nop 1
	v_addc_co_u32_e32 v231, vcc, 0, v231, vcc
	global_load_dwordx2 v[96:97], v[228:229], off
	global_load_dwordx2 v[98:99], v[228:229], off offset:512
	global_load_dwordx2 v[100:101], v[228:229], off offset:1024
	global_load_dwordx2 v[102:103], v[228:229], off offset:1536
	global_load_dwordx2 v[104:105], v[230:231], off offset:2048
	global_load_dwordx2 v[106:107], v[230:231], off offset:2560
	global_load_dwordx2 v[108:109], v[230:231], off offset:3072
	global_load_dwordx2 v[110:111], v[230:231], off offset:3584
	v_lshl_add_u64 v[228:229], v[228:229], 0, s[18:19]
	v_lshl_add_u64 v[230:231], v[230:231], 0, s[16:17]
	global_load_dwordx2 v[112:113], v[228:229], off
	global_load_dwordx2 v[114:115], v[228:229], off offset:512
	global_load_dwordx2 v[116:117], v[228:229], off offset:1024
	global_load_dwordx2 v[118:119], v[228:229], off offset:1536
	global_load_dwordx2 v[120:121], v[230:231], off offset:2048
	global_load_dwordx2 v[122:123], v[230:231], off offset:2560
	global_load_dwordx2 v[124:125], v[230:231], off offset:3072
	global_load_dwordx2 v[126:127], v[230:231], off offset:3584
	v_lshl_add_u64 v[228:229], v[228:229], 0, s[18:19]
	v_lshl_add_u64 v[230:231], v[230:231], 0, s[16:17]
	global_load_dwordx2 v[128:129], v[228:229], off
	global_load_dwordx2 v[130:131], v[228:229], off offset:512
	global_load_dwordx2 v[132:133], v[228:229], off offset:1024
	global_load_dwordx2 v[134:135], v[228:229], off offset:1536
	global_load_dwordx2 v[136:137], v[230:231], off offset:2048
	global_load_dwordx2 v[138:139], v[230:231], off offset:2560
	global_load_dwordx2 v[140:141], v[230:231], off offset:3072
	global_load_dwordx2 v[142:143], v[230:231], off offset:3584
	v_lshl_add_u64 v[228:229], v[228:229], 0, s[18:19]
	v_lshl_add_u64 v[230:231], v[230:231], 0, s[16:17]
	global_load_dwordx2 v[144:145], v[228:229], off
	global_load_dwordx2 v[146:147], v[228:229], off offset:512
	global_load_dwordx2 v[148:149], v[228:229], off offset:1024
	global_load_dwordx2 v[150:151], v[228:229], off offset:1536
	global_load_dwordx2 v[152:153], v[230:231], off offset:2048
	global_load_dwordx2 v[154:155], v[230:231], off offset:2560
	global_load_dwordx2 v[156:157], v[230:231], off offset:3072
	global_load_dwordx2 v[158:159], v[230:231], off offset:3584
	v_lshl_add_u64 v[228:229], v[228:229], 0, s[18:19]
	v_lshl_add_u64 v[230:231], v[230:231], 0, s[16:17]
	global_load_dwordx2 v[160:161], v[228:229], off
	global_load_dwordx2 v[162:163], v[228:229], off offset:512
	global_load_dwordx2 v[164:165], v[228:229], off offset:1024
	global_load_dwordx2 v[166:167], v[228:229], off offset:1536
	global_load_dwordx2 v[168:169], v[230:231], off offset:2048
	global_load_dwordx2 v[170:171], v[230:231], off offset:2560
	global_load_dwordx2 v[172:173], v[230:231], off offset:3072
	global_load_dwordx2 v[174:175], v[230:231], off offset:3584
	v_lshl_add_u64 v[228:229], v[228:229], 0, s[18:19]
	v_lshl_add_u64 v[230:231], v[230:231], 0, s[16:17]
	global_load_dwordx2 v[176:177], v[228:229], off
	global_load_dwordx2 v[178:179], v[228:229], off offset:512
	global_load_dwordx2 v[180:181], v[228:229], off offset:1024
	global_load_dwordx2 v[182:183], v[228:229], off offset:1536
	global_load_dwordx2 v[184:185], v[230:231], off offset:2048
	global_load_dwordx2 v[186:187], v[230:231], off offset:2560
	global_load_dwordx2 v[188:189], v[230:231], off offset:3072
	global_load_dwordx2 v[190:191], v[230:231], off offset:3584
	v_lshl_add_u64 v[228:229], v[228:229], 0, s[18:19]
	v_lshl_add_u64 v[230:231], v[230:231], 0, s[16:17]
	s_nop 0
	v_lshl_add_u64 v[30:31], v[24:25], 0, v[20:21]
	v_add_co_u32_e32 v40, vcc, 0x3ec4a000, v30
	v_lshl_add_u64 v[28:29], v[22:23], 0, v[20:21]
	v_add_co_u32_e64 v32, s[4:5], s23, v30
	v_addc_co_u32_e32 v41, vcc, 0, v31, vcc
	s_nop 0
	v_addc_co_u32_e64 v33, s[4:5], 0, v31, s[4:5]
	v_add_co_u32_e32 v28, vcc, 0x42c4b000, v28
	s_waitcnt vmcnt(40)
	v_mov_b32_e32 v30, v96
	v_mov_b32_e32 v31, v97
	v_mov_b32_e32 v42, v98
	v_mov_b32_e32 v43, v99
	v_mov_b32_e32 v44, v100
	v_mov_b32_e32 v45, v101
	v_mov_b32_e32 v46, v102
	v_mov_b32_e32 v47, v103
	v_mov_b32_e32 v40, v104
	v_mov_b32_e32 v41, v105
	v_mov_b32_e32 v48, v106
	v_mov_b32_e32 v49, v107
	v_mov_b32_e32 v50, v108
	v_mov_b32_e32 v51, v109
	v_mov_b32_e32 v52, v110
	v_mov_b32_e32 v53, v111
	global_load_dwordx2 v[192:193], v[228:229], off
	global_load_dwordx2 v[194:195], v[228:229], off offset:512
	global_load_dwordx2 v[196:197], v[228:229], off offset:1024
	global_load_dwordx2 v[198:199], v[228:229], off offset:1536
	global_load_dwordx2 v[200:201], v[230:231], off offset:2048
	global_load_dwordx2 v[202:203], v[230:231], off offset:2560
	global_load_dwordx2 v[204:205], v[230:231], off offset:3072
	global_load_dwordx2 v[206:207], v[230:231], off offset:3584
	v_lshl_add_u64 v[228:229], v[228:229], 0, s[18:19]
	v_lshl_add_u64 v[230:231], v[230:231], 0, s[16:17]
	v_addc_co_u32_e32 v29, vcc, 0, v29, vcc
	v_add_u32_e32 v18, s14, v18
	v_cmp_lt_i32_e64 s[4:5], s24, v18
	s_or_b64 s[20:21], s[4:5], s[20:21]
	v_lshl_add_u64 v[22:23], v[22:23], 0, s[16:17]
	v_lshl_add_u64 v[24:25], v[24:25], 0, s[18:19]
	s_nop 0
	v_lshlrev_b32_e32 v28, 16, v30
	v_and_b32_e32 v29, 0xffff0000, v30
	s_nop 0
	v_lshlrev_b32_e32 v54, 16, v42
	v_and_b32_e32 v55, 0xffff0000, v42
	v_and_b32_e32 v30, 0xffff0000, v31
	v_lshlrev_b32_e32 v31, 16, v31
	v_and_b32_e32 v42, 0xffff0000, v43
	v_lshlrev_b32_e32 v43, 16, v43
	v_pk_mul_f32 v[60:61], v[28:29], v[28:29]
	v_pk_mul_f32 v[64:65], v[54:55], v[54:55]
	s_nop 0
	v_lshlrev_b32_e32 v19, 16, v40
	v_and_b32_e32 v39, 0xffff0000, v40
	v_lshlrev_b32_e32 v40, 16, v41
	v_and_b32_e32 v41, 0xffff0000, v41
	v_lshlrev_b32_e32 v56, 16, v44
	v_and_b32_e32 v57, 0xffff0000, v44
	v_lshlrev_b32_e32 v58, 16, v46
	v_and_b32_e32 v59, 0xffff0000, v46
	v_pk_mul_f32 v[62:63], v[30:31], v[30:31]
	v_pk_mul_f32 v[66:67], v[42:43], v[42:43]
	v_mul_f32_e32 v86, 0xbfb8aa3b, v40
	v_mul_f32_e32 v87, 0xbfb8aa3b, v41
	v_mov_b32_e32 v40, v64
	v_mov_b32_e32 v41, v60
	v_mov_b32_e32 v60, v65
	v_and_b32_e32 v44, 0xffff0000, v45
	v_lshlrev_b32_e32 v45, 16, v45
	v_and_b32_e32 v46, 0xffff0000, v47
	v_lshlrev_b32_e32 v47, 16, v47
	v_pk_mul_f32 v[68:69], v[56:57], v[56:57]
	v_pk_mul_f32 v[72:73], v[58:59], v[58:59]
	s_nop 0
	v_lshlrev_b32_e32 v76, 16, v48
	v_and_b32_e32 v77, 0xffff0000, v48
	v_lshlrev_b32_e32 v78, 16, v49
	v_and_b32_e32 v79, 0xffff0000, v49
	s_nop 0
	v_lshlrev_b32_e32 v80, 16, v50
	v_and_b32_e32 v50, 0xffff0000, v50
	v_lshlrev_b32_e32 v81, 16, v51
	v_and_b32_e32 v51, 0xffff0000, v51
	v_mov_b32_e32 v48, v67
	v_mov_b32_e32 v49, v63
	v_pk_add_f32 v[40:41], v[40:41], v[60:61]
	v_pk_mul_f32 v[70:71], v[44:45], v[44:45]
	v_pk_mul_f32 v[74:75], v[46:47], v[46:47]
	v_mov_b32_e32 v67, v62
	v_mul_f32_e32 v63, 0xbfb8aa3b, v77
	v_mul_f32_e32 v65, 0xbfb8aa3b, v79
	v_mul_f32_e32 v77, 0xbfb8aa3b, v50
	v_mul_f32_e32 v79, 0xbfb8aa3b, v51
	v_mov_b32_e32 v50, v72
	v_mov_b32_e32 v51, v68
	v_mov_b32_e32 v68, v73
	v_pk_add_f32 v[40:41], v[48:49], v[40:41]
	s_nop 0
	v_lshlrev_b32_e32 v82, 16, v52
	v_and_b32_e32 v83, 0xffff0000, v52
	v_lshlrev_b32_e32 v84, 16, v53
	v_and_b32_e32 v85, 0xffff0000, v53
	v_mov_b32_e32 v52, v75
	v_mov_b32_e32 v53, v71
	v_pk_add_f32 v[50:51], v[50:51], v[68:69]
	v_pk_add_f32 v[40:41], v[66:67], v[40:41]
	v_pk_add_f32 v[48:49], v[52:53], v[50:51]
	ds_bpermute_b32 v51, v1, v41
	ds_bpermute_b32 v50, v1, v40
	v_mov_b32_e32 v75, v70
	v_pk_add_f32 v[48:49], v[74:75], v[48:49]
	ds_bpermute_b32 v53, v1, v49
	ds_bpermute_b32 v52, v1, v48
	s_waitcnt lgkmcnt(2)
	v_pk_add_f32 v[40:41], v[40:41], v[50:51]
	ds_bpermute_b32 v51, v34, v41
	ds_bpermute_b32 v50, v34, v40
	v_mul_f32_e32 v19, 0xbfb8aa3b, v19
	s_waitcnt lgkmcnt(2)
	v_pk_add_f32 v[48:49], v[48:49], v[52:53]
	ds_bpermute_b32 v53, v34, v49
	ds_bpermute_b32 v52, v34, v48
	s_waitcnt lgkmcnt(2)
	v_pk_add_f32 v[40:41], v[40:41], v[50:51]
	ds_bpermute_b32 v51, v35, v41
	ds_bpermute_b32 v50, v35, v40
	v_mul_f32_e32 v39, 0xbfb8aa3b, v39
	s_waitcnt lgkmcnt(2)
	v_pk_add_f32 v[48:49], v[48:49], v[52:53]
	ds_bpermute_b32 v53, v35, v49
	ds_bpermute_b32 v52, v35, v48
	s_waitcnt lgkmcnt(2)
	v_pk_add_f32 v[40:41], v[40:41], v[50:51]
	ds_bpermute_b32 v51, v36, v41
	ds_bpermute_b32 v50, v36, v40
	v_mul_f32_e32 v62, 0xbfb8aa3b, v76
	s_waitcnt lgkmcnt(2)
	v_pk_add_f32 v[48:49], v[48:49], v[52:53]
	ds_bpermute_b32 v53, v36, v49
	ds_bpermute_b32 v52, v36, v48
	s_waitcnt lgkmcnt(2)
	v_pk_add_f32 v[40:41], v[40:41], v[50:51]
	ds_bpermute_b32 v51, v37, v41
	ds_bpermute_b32 v50, v37, v40
	v_mul_f32_e32 v76, 0xbfb8aa3b, v80
	s_waitcnt lgkmcnt(2)
	v_pk_add_f32 v[48:49], v[48:49], v[52:53]
	ds_bpermute_b32 v53, v37, v49
	ds_bpermute_b32 v52, v37, v48
	s_waitcnt lgkmcnt(2)
	v_pk_add_f32 v[40:41], v[40:41], v[50:51]
	ds_bpermute_b32 v51, v38, v41
	ds_bpermute_b32 v50, v38, v40
	v_exp_f32_e32 v19, v19
	s_waitcnt lgkmcnt(2)
	v_pk_add_f32 v[48:49], v[48:49], v[52:53]
	ds_bpermute_b32 v53, v38, v49
	ds_bpermute_b32 v52, v38, v48
	s_waitcnt lgkmcnt(2)
	v_pk_add_f32 v[40:41], v[40:41], v[50:51]
	v_exp_f32_e32 v39, v39
	v_pk_fma_f32 v[40:41], v[40:41], s[22:23], v[26:27] op_sel_hi:[1,0,0]
	v_exp_f32_e32 v80, v86
	v_mul_f32_e32 v50, 0x4b800000, v41
	v_cmp_gt_f32_e64 s[8:9], s15, v41
	s_waitcnt lgkmcnt(0)
	v_pk_add_f32 v[48:49], v[48:49], v[52:53]
	v_mul_f32_e32 v64, 0xbfb8aa3b, v78
	v_cndmask_b32_e64 v41, v41, v50, s[8:9]
	v_mul_f32_e32 v78, 0xbfb8aa3b, v81
	v_exp_f32_e32 v81, v87
	v_pk_fma_f32 v[48:49], v[48:49], s[22:23], v[26:27] op_sel_hi:[1,0,0]
	v_mul_f32_e32 v51, 0x4b800000, v40
	v_cmp_gt_f32_e32 vcc, s15, v40
	v_rsq_f32_e32 v41, v41
	v_exp_f32_e32 v60, v62
	v_exp_f32_e32 v61, v63
	v_exp_f32_e32 v62, v64
	v_exp_f32_e32 v63, v65
	v_mul_f32_e32 v52, 0x4b800000, v49
	v_mul_f32_e32 v53, 0x4b800000, v48
	v_cmp_gt_f32_e64 s[4:5], s15, v48
	v_cmp_gt_f32_e64 s[6:7], s15, v49
	v_cndmask_b32_e32 v40, v40, v51, vcc
	v_mul_f32_e32 v70, 0xbfb8aa3b, v82
	v_mul_f32_e32 v71, 0xbfb8aa3b, v83
	v_mul_f32_e32 v72, 0xbfb8aa3b, v84
	v_mul_f32_e32 v73, 0xbfb8aa3b, v85
	v_exp_f32_e32 v64, v76
	v_exp_f32_e32 v65, v77
	v_exp_f32_e32 v76, v78
	v_exp_f32_e32 v77, v79
	v_cndmask_b32_e64 v49, v49, v52, s[6:7]
	v_cndmask_b32_e64 v48, v48, v53, s[4:5]
	v_rsq_f32_e32 v40, v40
	v_exp_f32_e32 v68, v70
	v_exp_f32_e32 v69, v71
	v_exp_f32_e32 v70, v72
	v_exp_f32_e32 v71, v73
	v_add_f32_e32 v19, 1.0, v19
	v_add_f32_e32 v39, 1.0, v39
	v_add_f32_e32 v66, 1.0, v80
	v_rsq_f32_e32 v49, v49
	v_rsq_f32_e32 v48, v48
	v_add_f32_e32 v67, 1.0, v81
	v_rcp_f32_e32 v19, v19
	v_rcp_f32_e32 v39, v39
	v_rcp_f32_e32 v66, v66
	v_mul_f32_e32 v50, 0x45800000, v41
	v_add_f32_e32 v60, 1.0, v60
	v_add_f32_e32 v61, 1.0, v61
	v_add_f32_e32 v62, 1.0, v62
	v_add_f32_e32 v63, 1.0, v63
	v_rcp_f32_e32 v67, v67
	v_cndmask_b32_e64 v41, v41, v50, s[8:9]
	v_add_f32_e32 v64, 1.0, v64
	v_add_f32_e32 v65, 1.0, v65
	v_add_f32_e32 v72, 1.0, v76
	v_add_f32_e32 v73, 1.0, v77
	v_rcp_f32_e32 v60, v60
	v_rcp_f32_e32 v61, v61
	v_rcp_f32_e32 v62, v62
	v_rcp_f32_e32 v63, v63
	v_mul_f32_e32 v51, 0x45800000, v40
	v_mul_f32_e32 v28, v41, v28
	v_mul_f32_e32 v29, v41, v29
	v_mul_f32_e32 v31, v41, v31
	v_add_f32_e32 v68, 1.0, v68
	v_add_f32_e32 v69, 1.0, v69
	v_add_f32_e32 v70, 1.0, v70
	v_add_f32_e32 v71, 1.0, v71
	v_rcp_f32_e32 v64, v64
	v_rcp_f32_e32 v65, v65
	v_rcp_f32_e32 v72, v72
	v_rcp_f32_e32 v73, v73
	v_mul_f32_e32 v52, 0x45800000, v49
	v_mul_f32_e32 v53, 0x45800000, v48
	v_cndmask_b32_e32 v40, v40, v51, vcc
	v_mul_f32_e32 v30, v41, v30
	v_mul_f32_e32 v28, v14, v28
	v_mul_f32_e32 v29, v15, v29
	v_mul_f32_e32 v31, v16, v31
	v_rcp_f32_e32 v68, v68
	v_rcp_f32_e32 v69, v69
	v_rcp_f32_e32 v70, v70
	v_rcp_f32_e32 v71, v71
	v_cndmask_b32_e64 v49, v49, v52, s[6:7]
	v_cndmask_b32_e64 v48, v48, v53, s[4:5]
	v_mul_f32_e32 v41, v40, v54
	v_mul_f32_e32 v50, v40, v55
	v_mul_f32_e32 v43, v40, v43
	v_mul_f32_e32 v40, v40, v42
	v_mul_f32_e32 v30, v17, v30
	v_mul_f32_e32 v19, v19, v28
	v_mul_f32_e32 v28, v39, v29
	v_mul_f32_e32 v29, v66, v31
	v_mul_f32_e32 v42, v49, v56
	v_mul_f32_e32 v51, v49, v57
	v_mul_f32_e32 v45, v49, v45
	v_mul_f32_e32 v44, v49, v44
	v_mul_f32_e32 v49, v48, v58
	v_mul_f32_e32 v52, v48, v59
	v_mul_f32_e32 v47, v48, v47
	v_mul_f32_e32 v46, v48, v46
	v_mul_f32_e32 v41, v10, v41
	v_mul_f32_e32 v48, v11, v50
	v_mul_f32_e32 v43, v12, v43
	v_mul_f32_e32 v40, v13, v40
	v_mul_f32_e32 v30, v67, v30
	v_cvt_pk_bf16_f32 v28, v19, v28
	v_cvt_pk_bf16_f32 v29, v29, v30
	v_mul_f32_e32 v42, v6, v42
	v_mul_f32_e32 v50, v7, v51
	v_mul_f32_e32 v45, v8, v45
	v_mul_f32_e32 v44, v9, v44
	v_mul_f32_e32 v31, v60, v41
	v_mul_f32_e32 v39, v61, v48
	v_mul_f32_e32 v41, v62, v43
	v_mul_f32_e32 v40, v63, v40
	global_store_dwordx2 v[32:33], v[28:29], off
	v_cvt_pk_bf16_f32 v28, v31, v39
	v_cvt_pk_bf16_f32 v29, v41, v40
	v_mul_f32_e32 v49, v2, v49
	v_mul_f32_e32 v51, v3, v52
	v_mul_f32_e32 v47, v4, v47
	v_mul_f32_e32 v46, v5, v46
	v_mul_f32_e32 v42, v64, v42
	v_mul_f32_e32 v43, v65, v50
	v_mul_f32_e32 v45, v72, v45
	v_mul_f32_e32 v44, v73, v44
	global_store_dwordx2 v[32:33], v[28:29], off offset:512
	v_cvt_pk_bf16_f32 v28, v42, v43
	v_cvt_pk_bf16_f32 v29, v45, v44
	v_mul_f32_e32 v48, v68, v49
	v_mul_f32_e32 v49, v69, v51
	v_mul_f32_e32 v47, v70, v47
	v_mul_f32_e32 v46, v71, v46
	global_store_dwordx2 v[32:33], v[28:29], off offset:1024
	v_cvt_pk_bf16_f32 v28, v48, v49
	v_cvt_pk_bf16_f32 v29, v47, v46
	global_store_dwordx2 v[32:33], v[28:29], off offset:1536
	s_andn2_b64 exec, exec, s[20:21]
	s_nop 0
	v_lshl_add_u64 v[30:31], v[24:25], 0, v[20:21]
	v_add_co_u32_e32 v40, vcc, 0x3ec4a000, v30
	v_lshl_add_u64 v[28:29], v[22:23], 0, v[20:21]
	v_add_co_u32_e64 v32, s[4:5], s23, v30
	v_addc_co_u32_e32 v41, vcc, 0, v31, vcc
	s_nop 0
	v_addc_co_u32_e64 v33, s[4:5], 0, v31, s[4:5]
	v_add_co_u32_e32 v28, vcc, 0x42c4b000, v28
	s_waitcnt vmcnt(44)
	v_mov_b32_e32 v30, v112
	v_mov_b32_e32 v31, v113
	v_mov_b32_e32 v42, v114
	v_mov_b32_e32 v43, v115
	v_mov_b32_e32 v44, v116
	v_mov_b32_e32 v45, v117
	v_mov_b32_e32 v46, v118
	v_mov_b32_e32 v47, v119
	v_mov_b32_e32 v40, v120
	v_mov_b32_e32 v41, v121
	v_mov_b32_e32 v48, v122
	v_mov_b32_e32 v49, v123
	v_mov_b32_e32 v50, v124
	v_mov_b32_e32 v51, v125
	v_mov_b32_e32 v52, v126
	v_mov_b32_e32 v53, v127
	global_load_dwordx2 v[208:209], v[228:229], off
	global_load_dwordx2 v[210:211], v[228:229], off offset:512
	global_load_dwordx2 v[212:213], v[228:229], off offset:1024
	global_load_dwordx2 v[214:215], v[228:229], off offset:1536
	global_load_dwordx2 v[216:217], v[230:231], off offset:2048
	global_load_dwordx2 v[218:219], v[230:231], off offset:2560
	global_load_dwordx2 v[220:221], v[230:231], off offset:3072
	global_load_dwordx2 v[222:223], v[230:231], off offset:3584
	v_lshl_add_u64 v[228:229], v[228:229], 0, s[18:19]
	v_lshl_add_u64 v[230:231], v[230:231], 0, s[16:17]
	v_addc_co_u32_e32 v29, vcc, 0, v29, vcc
	v_add_u32_e32 v18, s14, v18
	v_cmp_lt_i32_e64 s[4:5], s24, v18
	s_or_b64 s[20:21], s[4:5], s[20:21]
	v_lshl_add_u64 v[22:23], v[22:23], 0, s[16:17]
	v_lshl_add_u64 v[24:25], v[24:25], 0, s[18:19]
	s_nop 0
	v_lshlrev_b32_e32 v28, 16, v30
	v_and_b32_e32 v29, 0xffff0000, v30
	s_nop 0
	v_lshlrev_b32_e32 v54, 16, v42
	v_and_b32_e32 v55, 0xffff0000, v42
	v_and_b32_e32 v30, 0xffff0000, v31
	v_lshlrev_b32_e32 v31, 16, v31
	v_and_b32_e32 v42, 0xffff0000, v43
	v_lshlrev_b32_e32 v43, 16, v43
	v_pk_mul_f32 v[60:61], v[28:29], v[28:29]
	v_pk_mul_f32 v[64:65], v[54:55], v[54:55]
	s_nop 0
	v_lshlrev_b32_e32 v19, 16, v40
	v_and_b32_e32 v39, 0xffff0000, v40
	v_lshlrev_b32_e32 v40, 16, v41
	v_and_b32_e32 v41, 0xffff0000, v41
	v_lshlrev_b32_e32 v56, 16, v44
	v_and_b32_e32 v57, 0xffff0000, v44
	v_lshlrev_b32_e32 v58, 16, v46
	v_and_b32_e32 v59, 0xffff0000, v46
	v_pk_mul_f32 v[62:63], v[30:31], v[30:31]
	v_pk_mul_f32 v[66:67], v[42:43], v[42:43]
	v_mul_f32_e32 v86, 0xbfb8aa3b, v40
	v_mul_f32_e32 v87, 0xbfb8aa3b, v41
	v_mov_b32_e32 v40, v64
	v_mov_b32_e32 v41, v60
	v_mov_b32_e32 v60, v65
	v_and_b32_e32 v44, 0xffff0000, v45
	v_lshlrev_b32_e32 v45, 16, v45
	v_and_b32_e32 v46, 0xffff0000, v47
	v_lshlrev_b32_e32 v47, 16, v47
	v_pk_mul_f32 v[68:69], v[56:57], v[56:57]
	v_pk_mul_f32 v[72:73], v[58:59], v[58:59]
	s_nop 0
	v_lshlrev_b32_e32 v76, 16, v48
	v_and_b32_e32 v77, 0xffff0000, v48
	v_lshlrev_b32_e32 v78, 16, v49
	v_and_b32_e32 v79, 0xffff0000, v49
	s_nop 0
	v_lshlrev_b32_e32 v80, 16, v50
	v_and_b32_e32 v50, 0xffff0000, v50
	v_lshlrev_b32_e32 v81, 16, v51
	v_and_b32_e32 v51, 0xffff0000, v51
	v_mov_b32_e32 v48, v67
	v_mov_b32_e32 v49, v63
	v_pk_add_f32 v[40:41], v[40:41], v[60:61]
	v_pk_mul_f32 v[70:71], v[44:45], v[44:45]
	v_pk_mul_f32 v[74:75], v[46:47], v[46:47]
	v_mov_b32_e32 v67, v62
	v_mul_f32_e32 v63, 0xbfb8aa3b, v77
	v_mul_f32_e32 v65, 0xbfb8aa3b, v79
	v_mul_f32_e32 v77, 0xbfb8aa3b, v50
	v_mul_f32_e32 v79, 0xbfb8aa3b, v51
	v_mov_b32_e32 v50, v72
	v_mov_b32_e32 v51, v68
	v_mov_b32_e32 v68, v73
	v_pk_add_f32 v[40:41], v[48:49], v[40:41]
	s_nop 0
	v_lshlrev_b32_e32 v82, 16, v52
	v_and_b32_e32 v83, 0xffff0000, v52
	v_lshlrev_b32_e32 v84, 16, v53
	v_and_b32_e32 v85, 0xffff0000, v53
	v_mov_b32_e32 v52, v75
	v_mov_b32_e32 v53, v71
	v_pk_add_f32 v[50:51], v[50:51], v[68:69]
	v_pk_add_f32 v[40:41], v[66:67], v[40:41]
	v_pk_add_f32 v[48:49], v[52:53], v[50:51]
	ds_bpermute_b32 v51, v1, v41
	ds_bpermute_b32 v50, v1, v40
	v_mov_b32_e32 v75, v70
	v_pk_add_f32 v[48:49], v[74:75], v[48:49]
	ds_bpermute_b32 v53, v1, v49
	ds_bpermute_b32 v52, v1, v48
	s_waitcnt lgkmcnt(2)
	v_pk_add_f32 v[40:41], v[40:41], v[50:51]
	ds_bpermute_b32 v51, v34, v41
	ds_bpermute_b32 v50, v34, v40
	v_mul_f32_e32 v19, 0xbfb8aa3b, v19
	s_waitcnt lgkmcnt(2)
	v_pk_add_f32 v[48:49], v[48:49], v[52:53]
	ds_bpermute_b32 v53, v34, v49
	ds_bpermute_b32 v52, v34, v48
	s_waitcnt lgkmcnt(2)
	v_pk_add_f32 v[40:41], v[40:41], v[50:51]
	ds_bpermute_b32 v51, v35, v41
	ds_bpermute_b32 v50, v35, v40
	v_mul_f32_e32 v39, 0xbfb8aa3b, v39
	s_waitcnt lgkmcnt(2)
	v_pk_add_f32 v[48:49], v[48:49], v[52:53]
	ds_bpermute_b32 v53, v35, v49
	ds_bpermute_b32 v52, v35, v48
	s_waitcnt lgkmcnt(2)
	v_pk_add_f32 v[40:41], v[40:41], v[50:51]
	ds_bpermute_b32 v51, v36, v41
	ds_bpermute_b32 v50, v36, v40
	v_mul_f32_e32 v62, 0xbfb8aa3b, v76
	s_waitcnt lgkmcnt(2)
	v_pk_add_f32 v[48:49], v[48:49], v[52:53]
	ds_bpermute_b32 v53, v36, v49
	ds_bpermute_b32 v52, v36, v48
	s_waitcnt lgkmcnt(2)
	v_pk_add_f32 v[40:41], v[40:41], v[50:51]
	ds_bpermute_b32 v51, v37, v41
	ds_bpermute_b32 v50, v37, v40
	v_mul_f32_e32 v76, 0xbfb8aa3b, v80
	s_waitcnt lgkmcnt(2)
	v_pk_add_f32 v[48:49], v[48:49], v[52:53]
	ds_bpermute_b32 v53, v37, v49
	ds_bpermute_b32 v52, v37, v48
	s_waitcnt lgkmcnt(2)
	v_pk_add_f32 v[40:41], v[40:41], v[50:51]
	ds_bpermute_b32 v51, v38, v41
	ds_bpermute_b32 v50, v38, v40
	v_exp_f32_e32 v19, v19
	s_waitcnt lgkmcnt(2)
	v_pk_add_f32 v[48:49], v[48:49], v[52:53]
	ds_bpermute_b32 v53, v38, v49
	ds_bpermute_b32 v52, v38, v48
	s_waitcnt lgkmcnt(2)
	v_pk_add_f32 v[40:41], v[40:41], v[50:51]
	v_exp_f32_e32 v39, v39
	v_pk_fma_f32 v[40:41], v[40:41], s[22:23], v[26:27] op_sel_hi:[1,0,0]
	v_exp_f32_e32 v80, v86
	v_mul_f32_e32 v50, 0x4b800000, v41
	v_cmp_gt_f32_e64 s[8:9], s15, v41
	s_waitcnt lgkmcnt(0)
	v_pk_add_f32 v[48:49], v[48:49], v[52:53]
	v_mul_f32_e32 v64, 0xbfb8aa3b, v78
	v_cndmask_b32_e64 v41, v41, v50, s[8:9]
	v_mul_f32_e32 v78, 0xbfb8aa3b, v81
	v_exp_f32_e32 v81, v87
	v_pk_fma_f32 v[48:49], v[48:49], s[22:23], v[26:27] op_sel_hi:[1,0,0]
	v_mul_f32_e32 v51, 0x4b800000, v40
	v_cmp_gt_f32_e32 vcc, s15, v40
	v_rsq_f32_e32 v41, v41
	v_exp_f32_e32 v60, v62
	v_exp_f32_e32 v61, v63
	v_exp_f32_e32 v62, v64
	v_exp_f32_e32 v63, v65
	v_mul_f32_e32 v52, 0x4b800000, v49
	v_mul_f32_e32 v53, 0x4b800000, v48
	v_cmp_gt_f32_e64 s[4:5], s15, v48
	v_cmp_gt_f32_e64 s[6:7], s15, v49
	v_cndmask_b32_e32 v40, v40, v51, vcc
	v_mul_f32_e32 v70, 0xbfb8aa3b, v82
	v_mul_f32_e32 v71, 0xbfb8aa3b, v83
	v_mul_f32_e32 v72, 0xbfb8aa3b, v84
	v_mul_f32_e32 v73, 0xbfb8aa3b, v85
	v_exp_f32_e32 v64, v76
	v_exp_f32_e32 v65, v77
	v_exp_f32_e32 v76, v78
	v_exp_f32_e32 v77, v79
	v_cndmask_b32_e64 v49, v49, v52, s[6:7]
	v_cndmask_b32_e64 v48, v48, v53, s[4:5]
	v_rsq_f32_e32 v40, v40
	v_exp_f32_e32 v68, v70
	v_exp_f32_e32 v69, v71
	v_exp_f32_e32 v70, v72
	v_exp_f32_e32 v71, v73
	v_add_f32_e32 v19, 1.0, v19
	v_add_f32_e32 v39, 1.0, v39
	v_add_f32_e32 v66, 1.0, v80
	v_rsq_f32_e32 v49, v49
	v_rsq_f32_e32 v48, v48
	v_add_f32_e32 v67, 1.0, v81
	v_rcp_f32_e32 v19, v19
	v_rcp_f32_e32 v39, v39
	v_rcp_f32_e32 v66, v66
	v_mul_f32_e32 v50, 0x45800000, v41
	v_add_f32_e32 v60, 1.0, v60
	v_add_f32_e32 v61, 1.0, v61
	v_add_f32_e32 v62, 1.0, v62
	v_add_f32_e32 v63, 1.0, v63
	v_rcp_f32_e32 v67, v67
	v_cndmask_b32_e64 v41, v41, v50, s[8:9]
	v_add_f32_e32 v64, 1.0, v64
	v_add_f32_e32 v65, 1.0, v65
	v_add_f32_e32 v72, 1.0, v76
	v_add_f32_e32 v73, 1.0, v77
	v_rcp_f32_e32 v60, v60
	v_rcp_f32_e32 v61, v61
	v_rcp_f32_e32 v62, v62
	v_rcp_f32_e32 v63, v63
	v_mul_f32_e32 v51, 0x45800000, v40
	v_mul_f32_e32 v28, v41, v28
	v_mul_f32_e32 v29, v41, v29
	v_mul_f32_e32 v31, v41, v31
	v_add_f32_e32 v68, 1.0, v68
	v_add_f32_e32 v69, 1.0, v69
	v_add_f32_e32 v70, 1.0, v70
	v_add_f32_e32 v71, 1.0, v71
	v_rcp_f32_e32 v64, v64
	v_rcp_f32_e32 v65, v65
	v_rcp_f32_e32 v72, v72
	v_rcp_f32_e32 v73, v73
	v_mul_f32_e32 v52, 0x45800000, v49
	v_mul_f32_e32 v53, 0x45800000, v48
	v_cndmask_b32_e32 v40, v40, v51, vcc
	v_mul_f32_e32 v30, v41, v30
	v_mul_f32_e32 v28, v14, v28
	v_mul_f32_e32 v29, v15, v29
	v_mul_f32_e32 v31, v16, v31
	v_rcp_f32_e32 v68, v68
	v_rcp_f32_e32 v69, v69
	v_rcp_f32_e32 v70, v70
	v_rcp_f32_e32 v71, v71
	v_cndmask_b32_e64 v49, v49, v52, s[6:7]
	v_cndmask_b32_e64 v48, v48, v53, s[4:5]
	v_mul_f32_e32 v41, v40, v54
	v_mul_f32_e32 v50, v40, v55
	v_mul_f32_e32 v43, v40, v43
	v_mul_f32_e32 v40, v40, v42
	v_mul_f32_e32 v30, v17, v30
	v_mul_f32_e32 v19, v19, v28
	v_mul_f32_e32 v28, v39, v29
	v_mul_f32_e32 v29, v66, v31
	v_mul_f32_e32 v42, v49, v56
	v_mul_f32_e32 v51, v49, v57
	v_mul_f32_e32 v45, v49, v45
	v_mul_f32_e32 v44, v49, v44
	v_mul_f32_e32 v49, v48, v58
	v_mul_f32_e32 v52, v48, v59
	v_mul_f32_e32 v47, v48, v47
	v_mul_f32_e32 v46, v48, v46
	v_mul_f32_e32 v41, v10, v41
	v_mul_f32_e32 v48, v11, v50
	v_mul_f32_e32 v43, v12, v43
	v_mul_f32_e32 v40, v13, v40
	v_mul_f32_e32 v30, v67, v30
	v_cvt_pk_bf16_f32 v28, v19, v28
	v_cvt_pk_bf16_f32 v29, v29, v30
	v_mul_f32_e32 v42, v6, v42
	v_mul_f32_e32 v50, v7, v51
	v_mul_f32_e32 v45, v8, v45
	v_mul_f32_e32 v44, v9, v44
	v_mul_f32_e32 v31, v60, v41
	v_mul_f32_e32 v39, v61, v48
	v_mul_f32_e32 v41, v62, v43
	v_mul_f32_e32 v40, v63, v40
	global_store_dwordx2 v[32:33], v[28:29], off
	v_cvt_pk_bf16_f32 v28, v31, v39
	v_cvt_pk_bf16_f32 v29, v41, v40
	v_mul_f32_e32 v49, v2, v49
	v_mul_f32_e32 v51, v3, v52
	v_mul_f32_e32 v47, v4, v47
	v_mul_f32_e32 v46, v5, v46
	v_mul_f32_e32 v42, v64, v42
	v_mul_f32_e32 v43, v65, v50
	v_mul_f32_e32 v45, v72, v45
	v_mul_f32_e32 v44, v73, v44
	global_store_dwordx2 v[32:33], v[28:29], off offset:512
	v_cvt_pk_bf16_f32 v28, v42, v43
	v_cvt_pk_bf16_f32 v29, v45, v44
	v_mul_f32_e32 v48, v68, v49
	v_mul_f32_e32 v49, v69, v51
	v_mul_f32_e32 v47, v70, v47
	v_mul_f32_e32 v46, v71, v46
	global_store_dwordx2 v[32:33], v[28:29], off offset:1024
	v_cvt_pk_bf16_f32 v28, v48, v49
	v_cvt_pk_bf16_f32 v29, v47, v46
	global_store_dwordx2 v[32:33], v[28:29], off offset:1536
	s_andn2_b64 exec, exec, s[20:21]
	s_nop 0
	v_lshl_add_u64 v[30:31], v[24:25], 0, v[20:21]
	v_add_co_u32_e32 v40, vcc, 0x3ec4a000, v30
	v_lshl_add_u64 v[28:29], v[22:23], 0, v[20:21]
	v_add_co_u32_e64 v32, s[4:5], s23, v30
	v_addc_co_u32_e32 v41, vcc, 0, v31, vcc
	s_nop 0
	v_addc_co_u32_e64 v33, s[4:5], 0, v31, s[4:5]
	v_add_co_u32_e32 v28, vcc, 0x42c4b000, v28
	s_waitcnt vmcnt(48)
	v_mov_b32_e32 v30, v128
	v_mov_b32_e32 v31, v129
	v_mov_b32_e32 v42, v130
	v_mov_b32_e32 v43, v131
	v_mov_b32_e32 v44, v132
	v_mov_b32_e32 v45, v133
	v_mov_b32_e32 v46, v134
	v_mov_b32_e32 v47, v135
	v_mov_b32_e32 v40, v136
	v_mov_b32_e32 v41, v137
	v_mov_b32_e32 v48, v138
	v_mov_b32_e32 v49, v139
	v_mov_b32_e32 v50, v140
	v_mov_b32_e32 v51, v141
	v_mov_b32_e32 v52, v142
	v_mov_b32_e32 v53, v143
	v_addc_co_u32_e32 v29, vcc, 0, v29, vcc
	v_add_u32_e32 v18, s14, v18
	v_cmp_lt_i32_e64 s[4:5], s24, v18
	s_or_b64 s[20:21], s[4:5], s[20:21]
	v_lshl_add_u64 v[22:23], v[22:23], 0, s[16:17]
	v_lshl_add_u64 v[24:25], v[24:25], 0, s[18:19]
	s_nop 0
	v_lshlrev_b32_e32 v28, 16, v30
	v_and_b32_e32 v29, 0xffff0000, v30
	s_nop 0
	v_lshlrev_b32_e32 v54, 16, v42
	v_and_b32_e32 v55, 0xffff0000, v42
	v_and_b32_e32 v30, 0xffff0000, v31
	v_lshlrev_b32_e32 v31, 16, v31
	v_and_b32_e32 v42, 0xffff0000, v43
	v_lshlrev_b32_e32 v43, 16, v43
	v_pk_mul_f32 v[60:61], v[28:29], v[28:29]
	v_pk_mul_f32 v[64:65], v[54:55], v[54:55]
	s_nop 0
	v_lshlrev_b32_e32 v19, 16, v40
	v_and_b32_e32 v39, 0xffff0000, v40
	v_lshlrev_b32_e32 v40, 16, v41
	v_and_b32_e32 v41, 0xffff0000, v41
	v_lshlrev_b32_e32 v56, 16, v44
	v_and_b32_e32 v57, 0xffff0000, v44
	v_lshlrev_b32_e32 v58, 16, v46
	v_and_b32_e32 v59, 0xffff0000, v46
	v_pk_mul_f32 v[62:63], v[30:31], v[30:31]
	v_pk_mul_f32 v[66:67], v[42:43], v[42:43]
	v_mul_f32_e32 v86, 0xbfb8aa3b, v40
	v_mul_f32_e32 v87, 0xbfb8aa3b, v41
	v_mov_b32_e32 v40, v64
	v_mov_b32_e32 v41, v60
	v_mov_b32_e32 v60, v65
	v_and_b32_e32 v44, 0xffff0000, v45
	v_lshlrev_b32_e32 v45, 16, v45
	v_and_b32_e32 v46, 0xffff0000, v47
	v_lshlrev_b32_e32 v47, 16, v47
	v_pk_mul_f32 v[68:69], v[56:57], v[56:57]
	v_pk_mul_f32 v[72:73], v[58:59], v[58:59]
	s_nop 0
	v_lshlrev_b32_e32 v76, 16, v48
	v_and_b32_e32 v77, 0xffff0000, v48
	v_lshlrev_b32_e32 v78, 16, v49
	v_and_b32_e32 v79, 0xffff0000, v49
	s_nop 0
	v_lshlrev_b32_e32 v80, 16, v50
	v_and_b32_e32 v50, 0xffff0000, v50
	v_lshlrev_b32_e32 v81, 16, v51
	v_and_b32_e32 v51, 0xffff0000, v51
	v_mov_b32_e32 v48, v67
	v_mov_b32_e32 v49, v63
	v_pk_add_f32 v[40:41], v[40:41], v[60:61]
	v_pk_mul_f32 v[70:71], v[44:45], v[44:45]
	v_pk_mul_f32 v[74:75], v[46:47], v[46:47]
	v_mov_b32_e32 v67, v62
	v_mul_f32_e32 v63, 0xbfb8aa3b, v77
	v_mul_f32_e32 v65, 0xbfb8aa3b, v79
	v_mul_f32_e32 v77, 0xbfb8aa3b, v50
	v_mul_f32_e32 v79, 0xbfb8aa3b, v51
	v_mov_b32_e32 v50, v72
	v_mov_b32_e32 v51, v68
	v_mov_b32_e32 v68, v73
	v_pk_add_f32 v[40:41], v[48:49], v[40:41]
	s_nop 0
	v_lshlrev_b32_e32 v82, 16, v52
	v_and_b32_e32 v83, 0xffff0000, v52
	v_lshlrev_b32_e32 v84, 16, v53
	v_and_b32_e32 v85, 0xffff0000, v53
	v_mov_b32_e32 v52, v75
	v_mov_b32_e32 v53, v71
	v_pk_add_f32 v[50:51], v[50:51], v[68:69]
	v_pk_add_f32 v[40:41], v[66:67], v[40:41]
	v_pk_add_f32 v[48:49], v[52:53], v[50:51]
	ds_bpermute_b32 v51, v1, v41
	ds_bpermute_b32 v50, v1, v40
	v_mov_b32_e32 v75, v70
	v_pk_add_f32 v[48:49], v[74:75], v[48:49]
	ds_bpermute_b32 v53, v1, v49
	ds_bpermute_b32 v52, v1, v48
	s_waitcnt lgkmcnt(2)
	v_pk_add_f32 v[40:41], v[40:41], v[50:51]
	ds_bpermute_b32 v51, v34, v41
	ds_bpermute_b32 v50, v34, v40
	v_mul_f32_e32 v19, 0xbfb8aa3b, v19
	s_waitcnt lgkmcnt(2)
	v_pk_add_f32 v[48:49], v[48:49], v[52:53]
	ds_bpermute_b32 v53, v34, v49
	ds_bpermute_b32 v52, v34, v48
	s_waitcnt lgkmcnt(2)
	v_pk_add_f32 v[40:41], v[40:41], v[50:51]
	ds_bpermute_b32 v51, v35, v41
	ds_bpermute_b32 v50, v35, v40
	v_mul_f32_e32 v39, 0xbfb8aa3b, v39
	s_waitcnt lgkmcnt(2)
	v_pk_add_f32 v[48:49], v[48:49], v[52:53]
	ds_bpermute_b32 v53, v35, v49
	ds_bpermute_b32 v52, v35, v48
	s_waitcnt lgkmcnt(2)
	v_pk_add_f32 v[40:41], v[40:41], v[50:51]
	ds_bpermute_b32 v51, v36, v41
	ds_bpermute_b32 v50, v36, v40
	v_mul_f32_e32 v62, 0xbfb8aa3b, v76
	s_waitcnt lgkmcnt(2)
	v_pk_add_f32 v[48:49], v[48:49], v[52:53]
	ds_bpermute_b32 v53, v36, v49
	ds_bpermute_b32 v52, v36, v48
	s_waitcnt lgkmcnt(2)
	v_pk_add_f32 v[40:41], v[40:41], v[50:51]
	ds_bpermute_b32 v51, v37, v41
	ds_bpermute_b32 v50, v37, v40
	v_mul_f32_e32 v76, 0xbfb8aa3b, v80
	s_waitcnt lgkmcnt(2)
	v_pk_add_f32 v[48:49], v[48:49], v[52:53]
	ds_bpermute_b32 v53, v37, v49
	ds_bpermute_b32 v52, v37, v48
	s_waitcnt lgkmcnt(2)
	v_pk_add_f32 v[40:41], v[40:41], v[50:51]
	ds_bpermute_b32 v51, v38, v41
	ds_bpermute_b32 v50, v38, v40
	v_exp_f32_e32 v19, v19
	s_waitcnt lgkmcnt(2)
	v_pk_add_f32 v[48:49], v[48:49], v[52:53]
	ds_bpermute_b32 v53, v38, v49
	ds_bpermute_b32 v52, v38, v48
	s_waitcnt lgkmcnt(2)
	v_pk_add_f32 v[40:41], v[40:41], v[50:51]
	v_exp_f32_e32 v39, v39
	v_pk_fma_f32 v[40:41], v[40:41], s[22:23], v[26:27] op_sel_hi:[1,0,0]
	v_exp_f32_e32 v80, v86
	v_mul_f32_e32 v50, 0x4b800000, v41
	v_cmp_gt_f32_e64 s[8:9], s15, v41
	s_waitcnt lgkmcnt(0)
	v_pk_add_f32 v[48:49], v[48:49], v[52:53]
	v_mul_f32_e32 v64, 0xbfb8aa3b, v78
	v_cndmask_b32_e64 v41, v41, v50, s[8:9]
	v_mul_f32_e32 v78, 0xbfb8aa3b, v81
	v_exp_f32_e32 v81, v87
	v_pk_fma_f32 v[48:49], v[48:49], s[22:23], v[26:27] op_sel_hi:[1,0,0]
	v_mul_f32_e32 v51, 0x4b800000, v40
	v_cmp_gt_f32_e32 vcc, s15, v40
	v_rsq_f32_e32 v41, v41
	v_exp_f32_e32 v60, v62
	v_exp_f32_e32 v61, v63
	v_exp_f32_e32 v62, v64
	v_exp_f32_e32 v63, v65
	v_mul_f32_e32 v52, 0x4b800000, v49
	v_mul_f32_e32 v53, 0x4b800000, v48
	v_cmp_gt_f32_e64 s[4:5], s15, v48
	v_cmp_gt_f32_e64 s[6:7], s15, v49
	v_cndmask_b32_e32 v40, v40, v51, vcc
	v_mul_f32_e32 v70, 0xbfb8aa3b, v82
	v_mul_f32_e32 v71, 0xbfb8aa3b, v83
	v_mul_f32_e32 v72, 0xbfb8aa3b, v84
	v_mul_f32_e32 v73, 0xbfb8aa3b, v85
	v_exp_f32_e32 v64, v76
	v_exp_f32_e32 v65, v77
	v_exp_f32_e32 v76, v78
	v_exp_f32_e32 v77, v79
	v_cndmask_b32_e64 v49, v49, v52, s[6:7]
	v_cndmask_b32_e64 v48, v48, v53, s[4:5]
	v_rsq_f32_e32 v40, v40
	v_exp_f32_e32 v68, v70
	v_exp_f32_e32 v69, v71
	v_exp_f32_e32 v70, v72
	v_exp_f32_e32 v71, v73
	v_add_f32_e32 v19, 1.0, v19
	v_add_f32_e32 v39, 1.0, v39
	v_add_f32_e32 v66, 1.0, v80
	v_rsq_f32_e32 v49, v49
	v_rsq_f32_e32 v48, v48
	v_add_f32_e32 v67, 1.0, v81
	v_rcp_f32_e32 v19, v19
	v_rcp_f32_e32 v39, v39
	v_rcp_f32_e32 v66, v66
	v_mul_f32_e32 v50, 0x45800000, v41
	v_add_f32_e32 v60, 1.0, v60
	v_add_f32_e32 v61, 1.0, v61
	v_add_f32_e32 v62, 1.0, v62
	v_add_f32_e32 v63, 1.0, v63
	v_rcp_f32_e32 v67, v67
	v_cndmask_b32_e64 v41, v41, v50, s[8:9]
	v_add_f32_e32 v64, 1.0, v64
	v_add_f32_e32 v65, 1.0, v65
	v_add_f32_e32 v72, 1.0, v76
	v_add_f32_e32 v73, 1.0, v77
	v_rcp_f32_e32 v60, v60
	v_rcp_f32_e32 v61, v61
	v_rcp_f32_e32 v62, v62
	v_rcp_f32_e32 v63, v63
	v_mul_f32_e32 v51, 0x45800000, v40
	v_mul_f32_e32 v28, v41, v28
	v_mul_f32_e32 v29, v41, v29
	v_mul_f32_e32 v31, v41, v31
	v_add_f32_e32 v68, 1.0, v68
	v_add_f32_e32 v69, 1.0, v69
	v_add_f32_e32 v70, 1.0, v70
	v_add_f32_e32 v71, 1.0, v71
	v_rcp_f32_e32 v64, v64
	v_rcp_f32_e32 v65, v65
	v_rcp_f32_e32 v72, v72
	v_rcp_f32_e32 v73, v73
	v_mul_f32_e32 v52, 0x45800000, v49
	v_mul_f32_e32 v53, 0x45800000, v48
	v_cndmask_b32_e32 v40, v40, v51, vcc
	v_mul_f32_e32 v30, v41, v30
	v_mul_f32_e32 v28, v14, v28
	v_mul_f32_e32 v29, v15, v29
	v_mul_f32_e32 v31, v16, v31
	v_rcp_f32_e32 v68, v68
	v_rcp_f32_e32 v69, v69
	v_rcp_f32_e32 v70, v70
	v_rcp_f32_e32 v71, v71
	v_cndmask_b32_e64 v49, v49, v52, s[6:7]
	v_cndmask_b32_e64 v48, v48, v53, s[4:5]
	v_mul_f32_e32 v41, v40, v54
	v_mul_f32_e32 v50, v40, v55
	v_mul_f32_e32 v43, v40, v43
	v_mul_f32_e32 v40, v40, v42
	v_mul_f32_e32 v30, v17, v30
	v_mul_f32_e32 v19, v19, v28
	v_mul_f32_e32 v28, v39, v29
	v_mul_f32_e32 v29, v66, v31
	v_mul_f32_e32 v42, v49, v56
	v_mul_f32_e32 v51, v49, v57
	v_mul_f32_e32 v45, v49, v45
	v_mul_f32_e32 v44, v49, v44
	v_mul_f32_e32 v49, v48, v58
	v_mul_f32_e32 v52, v48, v59
	v_mul_f32_e32 v47, v48, v47
	v_mul_f32_e32 v46, v48, v46
	v_mul_f32_e32 v41, v10, v41
	v_mul_f32_e32 v48, v11, v50
	v_mul_f32_e32 v43, v12, v43
	v_mul_f32_e32 v40, v13, v40
	v_mul_f32_e32 v30, v67, v30
	v_cvt_pk_bf16_f32 v28, v19, v28
	v_cvt_pk_bf16_f32 v29, v29, v30
	v_mul_f32_e32 v42, v6, v42
	v_mul_f32_e32 v50, v7, v51
	v_mul_f32_e32 v45, v8, v45
	v_mul_f32_e32 v44, v9, v44
	v_mul_f32_e32 v31, v60, v41
	v_mul_f32_e32 v39, v61, v48
	v_mul_f32_e32 v41, v62, v43
	v_mul_f32_e32 v40, v63, v40
	global_store_dwordx2 v[32:33], v[28:29], off
	v_cvt_pk_bf16_f32 v28, v31, v39
	v_cvt_pk_bf16_f32 v29, v41, v40
	v_mul_f32_e32 v49, v2, v49
	v_mul_f32_e32 v51, v3, v52
	v_mul_f32_e32 v47, v4, v47
	v_mul_f32_e32 v46, v5, v46
	v_mul_f32_e32 v42, v64, v42
	v_mul_f32_e32 v43, v65, v50
	v_mul_f32_e32 v45, v72, v45
	v_mul_f32_e32 v44, v73, v44
	global_store_dwordx2 v[32:33], v[28:29], off offset:512
	v_cvt_pk_bf16_f32 v28, v42, v43
	v_cvt_pk_bf16_f32 v29, v45, v44
	v_mul_f32_e32 v48, v68, v49
	v_mul_f32_e32 v49, v69, v51
	v_mul_f32_e32 v47, v70, v47
	v_mul_f32_e32 v46, v71, v46
	global_store_dwordx2 v[32:33], v[28:29], off offset:1024
	v_cvt_pk_bf16_f32 v28, v48, v49
	v_cvt_pk_bf16_f32 v29, v47, v46
	global_store_dwordx2 v[32:33], v[28:29], off offset:1536
	s_andn2_b64 exec, exec, s[20:21]
	s_nop 0
	v_lshl_add_u64 v[30:31], v[24:25], 0, v[20:21]
	v_add_co_u32_e32 v40, vcc, 0x3ec4a000, v30
	v_lshl_add_u64 v[28:29], v[22:23], 0, v[20:21]
	v_add_co_u32_e64 v32, s[4:5], s23, v30
	v_addc_co_u32_e32 v41, vcc, 0, v31, vcc
	s_nop 0
	v_addc_co_u32_e64 v33, s[4:5], 0, v31, s[4:5]
	v_add_co_u32_e32 v28, vcc, 0x42c4b000, v28
	s_waitcnt vmcnt(44)
	v_mov_b32_e32 v30, v144
	v_mov_b32_e32 v31, v145
	v_mov_b32_e32 v42, v146
	v_mov_b32_e32 v43, v147
	v_mov_b32_e32 v44, v148
	v_mov_b32_e32 v45, v149
	v_mov_b32_e32 v46, v150
	v_mov_b32_e32 v47, v151
	v_mov_b32_e32 v40, v152
	v_mov_b32_e32 v41, v153
	v_mov_b32_e32 v48, v154
	v_mov_b32_e32 v49, v155
	v_mov_b32_e32 v50, v156
	v_mov_b32_e32 v51, v157
	v_mov_b32_e32 v52, v158
	v_mov_b32_e32 v53, v159
	v_addc_co_u32_e32 v29, vcc, 0, v29, vcc
	v_add_u32_e32 v18, s14, v18
	v_cmp_lt_i32_e64 s[4:5], s24, v18
	s_or_b64 s[20:21], s[4:5], s[20:21]
	v_lshl_add_u64 v[22:23], v[22:23], 0, s[16:17]
	v_lshl_add_u64 v[24:25], v[24:25], 0, s[18:19]
	s_nop 0
	v_lshlrev_b32_e32 v28, 16, v30
	v_and_b32_e32 v29, 0xffff0000, v30
	s_nop 0
	v_lshlrev_b32_e32 v54, 16, v42
	v_and_b32_e32 v55, 0xffff0000, v42
	v_and_b32_e32 v30, 0xffff0000, v31
	v_lshlrev_b32_e32 v31, 16, v31
	v_and_b32_e32 v42, 0xffff0000, v43
	v_lshlrev_b32_e32 v43, 16, v43
	v_pk_mul_f32 v[60:61], v[28:29], v[28:29]
	v_pk_mul_f32 v[64:65], v[54:55], v[54:55]
	s_nop 0
	v_lshlrev_b32_e32 v19, 16, v40
	v_and_b32_e32 v39, 0xffff0000, v40
	v_lshlrev_b32_e32 v40, 16, v41
	v_and_b32_e32 v41, 0xffff0000, v41
	v_lshlrev_b32_e32 v56, 16, v44
	v_and_b32_e32 v57, 0xffff0000, v44
	v_lshlrev_b32_e32 v58, 16, v46
	v_and_b32_e32 v59, 0xffff0000, v46
	v_pk_mul_f32 v[62:63], v[30:31], v[30:31]
	v_pk_mul_f32 v[66:67], v[42:43], v[42:43]
	v_mul_f32_e32 v86, 0xbfb8aa3b, v40
	v_mul_f32_e32 v87, 0xbfb8aa3b, v41
	v_mov_b32_e32 v40, v64
	v_mov_b32_e32 v41, v60
	v_mov_b32_e32 v60, v65
	v_and_b32_e32 v44, 0xffff0000, v45
	v_lshlrev_b32_e32 v45, 16, v45
	v_and_b32_e32 v46, 0xffff0000, v47
	v_lshlrev_b32_e32 v47, 16, v47
	v_pk_mul_f32 v[68:69], v[56:57], v[56:57]
	v_pk_mul_f32 v[72:73], v[58:59], v[58:59]
	s_nop 0
	v_lshlrev_b32_e32 v76, 16, v48
	v_and_b32_e32 v77, 0xffff0000, v48
	v_lshlrev_b32_e32 v78, 16, v49
	v_and_b32_e32 v79, 0xffff0000, v49
	s_nop 0
	v_lshlrev_b32_e32 v80, 16, v50
	v_and_b32_e32 v50, 0xffff0000, v50
	v_lshlrev_b32_e32 v81, 16, v51
	v_and_b32_e32 v51, 0xffff0000, v51
	v_mov_b32_e32 v48, v67
	v_mov_b32_e32 v49, v63
	v_pk_add_f32 v[40:41], v[40:41], v[60:61]
	v_pk_mul_f32 v[70:71], v[44:45], v[44:45]
	v_pk_mul_f32 v[74:75], v[46:47], v[46:47]
	v_mov_b32_e32 v67, v62
	v_mul_f32_e32 v63, 0xbfb8aa3b, v77
	v_mul_f32_e32 v65, 0xbfb8aa3b, v79
	v_mul_f32_e32 v77, 0xbfb8aa3b, v50
	v_mul_f32_e32 v79, 0xbfb8aa3b, v51
	v_mov_b32_e32 v50, v72
	v_mov_b32_e32 v51, v68
	v_mov_b32_e32 v68, v73
	v_pk_add_f32 v[40:41], v[48:49], v[40:41]
	s_nop 0
	v_lshlrev_b32_e32 v82, 16, v52
	v_and_b32_e32 v83, 0xffff0000, v52
	v_lshlrev_b32_e32 v84, 16, v53
	v_and_b32_e32 v85, 0xffff0000, v53
	v_mov_b32_e32 v52, v75
	v_mov_b32_e32 v53, v71
	v_pk_add_f32 v[50:51], v[50:51], v[68:69]
	v_pk_add_f32 v[40:41], v[66:67], v[40:41]
	v_pk_add_f32 v[48:49], v[52:53], v[50:51]
	ds_bpermute_b32 v51, v1, v41
	ds_bpermute_b32 v50, v1, v40
	v_mov_b32_e32 v75, v70
	v_pk_add_f32 v[48:49], v[74:75], v[48:49]
	ds_bpermute_b32 v53, v1, v49
	ds_bpermute_b32 v52, v1, v48
	s_waitcnt lgkmcnt(2)
	v_pk_add_f32 v[40:41], v[40:41], v[50:51]
	ds_bpermute_b32 v51, v34, v41
	ds_bpermute_b32 v50, v34, v40
	v_mul_f32_e32 v19, 0xbfb8aa3b, v19
	s_waitcnt lgkmcnt(2)
	v_pk_add_f32 v[48:49], v[48:49], v[52:53]
	ds_bpermute_b32 v53, v34, v49
	ds_bpermute_b32 v52, v34, v48
	s_waitcnt lgkmcnt(2)
	v_pk_add_f32 v[40:41], v[40:41], v[50:51]
	ds_bpermute_b32 v51, v35, v41
	ds_bpermute_b32 v50, v35, v40
	v_mul_f32_e32 v39, 0xbfb8aa3b, v39
	s_waitcnt lgkmcnt(2)
	v_pk_add_f32 v[48:49], v[48:49], v[52:53]
	ds_bpermute_b32 v53, v35, v49
	ds_bpermute_b32 v52, v35, v48
	s_waitcnt lgkmcnt(2)
	v_pk_add_f32 v[40:41], v[40:41], v[50:51]
	ds_bpermute_b32 v51, v36, v41
	ds_bpermute_b32 v50, v36, v40
	v_mul_f32_e32 v62, 0xbfb8aa3b, v76
	s_waitcnt lgkmcnt(2)
	v_pk_add_f32 v[48:49], v[48:49], v[52:53]
	ds_bpermute_b32 v53, v36, v49
	ds_bpermute_b32 v52, v36, v48
	s_waitcnt lgkmcnt(2)
	v_pk_add_f32 v[40:41], v[40:41], v[50:51]
	ds_bpermute_b32 v51, v37, v41
	ds_bpermute_b32 v50, v37, v40
	v_mul_f32_e32 v76, 0xbfb8aa3b, v80
	s_waitcnt lgkmcnt(2)
	v_pk_add_f32 v[48:49], v[48:49], v[52:53]
	ds_bpermute_b32 v53, v37, v49
	ds_bpermute_b32 v52, v37, v48
	s_waitcnt lgkmcnt(2)
	v_pk_add_f32 v[40:41], v[40:41], v[50:51]
	ds_bpermute_b32 v51, v38, v41
	ds_bpermute_b32 v50, v38, v40
	v_exp_f32_e32 v19, v19
	s_waitcnt lgkmcnt(2)
	v_pk_add_f32 v[48:49], v[48:49], v[52:53]
	ds_bpermute_b32 v53, v38, v49
	ds_bpermute_b32 v52, v38, v48
	s_waitcnt lgkmcnt(2)
	v_pk_add_f32 v[40:41], v[40:41], v[50:51]
	v_exp_f32_e32 v39, v39
	v_pk_fma_f32 v[40:41], v[40:41], s[22:23], v[26:27] op_sel_hi:[1,0,0]
	v_exp_f32_e32 v80, v86
	v_mul_f32_e32 v50, 0x4b800000, v41
	v_cmp_gt_f32_e64 s[8:9], s15, v41
	s_waitcnt lgkmcnt(0)
	v_pk_add_f32 v[48:49], v[48:49], v[52:53]
	v_mul_f32_e32 v64, 0xbfb8aa3b, v78
	v_cndmask_b32_e64 v41, v41, v50, s[8:9]
	v_mul_f32_e32 v78, 0xbfb8aa3b, v81
	v_exp_f32_e32 v81, v87
	v_pk_fma_f32 v[48:49], v[48:49], s[22:23], v[26:27] op_sel_hi:[1,0,0]
	v_mul_f32_e32 v51, 0x4b800000, v40
	v_cmp_gt_f32_e32 vcc, s15, v40
	v_rsq_f32_e32 v41, v41
	v_exp_f32_e32 v60, v62
	v_exp_f32_e32 v61, v63
	v_exp_f32_e32 v62, v64
	v_exp_f32_e32 v63, v65
	v_mul_f32_e32 v52, 0x4b800000, v49
	v_mul_f32_e32 v53, 0x4b800000, v48
	v_cmp_gt_f32_e64 s[4:5], s15, v48
	v_cmp_gt_f32_e64 s[6:7], s15, v49
	v_cndmask_b32_e32 v40, v40, v51, vcc
	v_mul_f32_e32 v70, 0xbfb8aa3b, v82
	v_mul_f32_e32 v71, 0xbfb8aa3b, v83
	v_mul_f32_e32 v72, 0xbfb8aa3b, v84
	v_mul_f32_e32 v73, 0xbfb8aa3b, v85
	v_exp_f32_e32 v64, v76
	v_exp_f32_e32 v65, v77
	v_exp_f32_e32 v76, v78
	v_exp_f32_e32 v77, v79
	v_cndmask_b32_e64 v49, v49, v52, s[6:7]
	v_cndmask_b32_e64 v48, v48, v53, s[4:5]
	v_rsq_f32_e32 v40, v40
	v_exp_f32_e32 v68, v70
	v_exp_f32_e32 v69, v71
	v_exp_f32_e32 v70, v72
	v_exp_f32_e32 v71, v73
	v_add_f32_e32 v19, 1.0, v19
	v_add_f32_e32 v39, 1.0, v39
	v_add_f32_e32 v66, 1.0, v80
	v_rsq_f32_e32 v49, v49
	v_rsq_f32_e32 v48, v48
	v_add_f32_e32 v67, 1.0, v81
	v_rcp_f32_e32 v19, v19
	v_rcp_f32_e32 v39, v39
	v_rcp_f32_e32 v66, v66
	v_mul_f32_e32 v50, 0x45800000, v41
	v_add_f32_e32 v60, 1.0, v60
	v_add_f32_e32 v61, 1.0, v61
	v_add_f32_e32 v62, 1.0, v62
	v_add_f32_e32 v63, 1.0, v63
	v_rcp_f32_e32 v67, v67
	v_cndmask_b32_e64 v41, v41, v50, s[8:9]
	v_add_f32_e32 v64, 1.0, v64
	v_add_f32_e32 v65, 1.0, v65
	v_add_f32_e32 v72, 1.0, v76
	v_add_f32_e32 v73, 1.0, v77
	v_rcp_f32_e32 v60, v60
	v_rcp_f32_e32 v61, v61
	v_rcp_f32_e32 v62, v62
	v_rcp_f32_e32 v63, v63
	v_mul_f32_e32 v51, 0x45800000, v40
	v_mul_f32_e32 v28, v41, v28
	v_mul_f32_e32 v29, v41, v29
	v_mul_f32_e32 v31, v41, v31
	v_add_f32_e32 v68, 1.0, v68
	v_add_f32_e32 v69, 1.0, v69
	v_add_f32_e32 v70, 1.0, v70
	v_add_f32_e32 v71, 1.0, v71
	v_rcp_f32_e32 v64, v64
	v_rcp_f32_e32 v65, v65
	v_rcp_f32_e32 v72, v72
	v_rcp_f32_e32 v73, v73
	v_mul_f32_e32 v52, 0x45800000, v49
	v_mul_f32_e32 v53, 0x45800000, v48
	v_cndmask_b32_e32 v40, v40, v51, vcc
	v_mul_f32_e32 v30, v41, v30
	v_mul_f32_e32 v28, v14, v28
	v_mul_f32_e32 v29, v15, v29
	v_mul_f32_e32 v31, v16, v31
	v_rcp_f32_e32 v68, v68
	v_rcp_f32_e32 v69, v69
	v_rcp_f32_e32 v70, v70
	v_rcp_f32_e32 v71, v71
	v_cndmask_b32_e64 v49, v49, v52, s[6:7]
	v_cndmask_b32_e64 v48, v48, v53, s[4:5]
	v_mul_f32_e32 v41, v40, v54
	v_mul_f32_e32 v50, v40, v55
	v_mul_f32_e32 v43, v40, v43
	v_mul_f32_e32 v40, v40, v42
	v_mul_f32_e32 v30, v17, v30
	v_mul_f32_e32 v19, v19, v28
	v_mul_f32_e32 v28, v39, v29
	v_mul_f32_e32 v29, v66, v31
	v_mul_f32_e32 v42, v49, v56
	v_mul_f32_e32 v51, v49, v57
	v_mul_f32_e32 v45, v49, v45
	v_mul_f32_e32 v44, v49, v44
	v_mul_f32_e32 v49, v48, v58
	v_mul_f32_e32 v52, v48, v59
	v_mul_f32_e32 v47, v48, v47
	v_mul_f32_e32 v46, v48, v46
	v_mul_f32_e32 v41, v10, v41
	v_mul_f32_e32 v48, v11, v50
	v_mul_f32_e32 v43, v12, v43
	v_mul_f32_e32 v40, v13, v40
	v_mul_f32_e32 v30, v67, v30
	v_cvt_pk_bf16_f32 v28, v19, v28
	v_cvt_pk_bf16_f32 v29, v29, v30
	v_mul_f32_e32 v42, v6, v42
	v_mul_f32_e32 v50, v7, v51
	v_mul_f32_e32 v45, v8, v45
	v_mul_f32_e32 v44, v9, v44
	v_mul_f32_e32 v31, v60, v41
	v_mul_f32_e32 v39, v61, v48
	v_mul_f32_e32 v41, v62, v43
	v_mul_f32_e32 v40, v63, v40
	global_store_dwordx2 v[32:33], v[28:29], off
	v_cvt_pk_bf16_f32 v28, v31, v39
	v_cvt_pk_bf16_f32 v29, v41, v40
	v_mul_f32_e32 v49, v2, v49
	v_mul_f32_e32 v51, v3, v52
	v_mul_f32_e32 v47, v4, v47
	v_mul_f32_e32 v46, v5, v46
	v_mul_f32_e32 v42, v64, v42
	v_mul_f32_e32 v43, v65, v50
	v_mul_f32_e32 v45, v72, v45
	v_mul_f32_e32 v44, v73, v44
	global_store_dwordx2 v[32:33], v[28:29], off offset:512
	v_cvt_pk_bf16_f32 v28, v42, v43
	v_cvt_pk_bf16_f32 v29, v45, v44
	v_mul_f32_e32 v48, v68, v49
	v_mul_f32_e32 v49, v69, v51
	v_mul_f32_e32 v47, v70, v47
	v_mul_f32_e32 v46, v71, v46
	global_store_dwordx2 v[32:33], v[28:29], off offset:1024
	v_cvt_pk_bf16_f32 v28, v48, v49
	v_cvt_pk_bf16_f32 v29, v47, v46
	global_store_dwordx2 v[32:33], v[28:29], off offset:1536
	s_andn2_b64 exec, exec, s[20:21]
	s_nop 0
	v_lshl_add_u64 v[30:31], v[24:25], 0, v[20:21]
	v_add_co_u32_e32 v40, vcc, 0x3ec4a000, v30
	v_lshl_add_u64 v[28:29], v[22:23], 0, v[20:21]
	v_add_co_u32_e64 v32, s[4:5], s23, v30
	v_addc_co_u32_e32 v41, vcc, 0, v31, vcc
	s_nop 0
	v_addc_co_u32_e64 v33, s[4:5], 0, v31, s[4:5]
	v_add_co_u32_e32 v28, vcc, 0x42c4b000, v28
	s_waitcnt vmcnt(40)
	v_mov_b32_e32 v30, v160
	v_mov_b32_e32 v31, v161
	v_mov_b32_e32 v42, v162
	v_mov_b32_e32 v43, v163
	v_mov_b32_e32 v44, v164
	v_mov_b32_e32 v45, v165
	v_mov_b32_e32 v46, v166
	v_mov_b32_e32 v47, v167
	v_mov_b32_e32 v40, v168
	v_mov_b32_e32 v41, v169
	v_mov_b32_e32 v48, v170
	v_mov_b32_e32 v49, v171
	v_mov_b32_e32 v50, v172
	v_mov_b32_e32 v51, v173
	v_mov_b32_e32 v52, v174
	v_mov_b32_e32 v53, v175
	v_addc_co_u32_e32 v29, vcc, 0, v29, vcc
	v_add_u32_e32 v18, s14, v18
	v_cmp_lt_i32_e64 s[4:5], s24, v18
	s_or_b64 s[20:21], s[4:5], s[20:21]
	v_lshl_add_u64 v[22:23], v[22:23], 0, s[16:17]
	v_lshl_add_u64 v[24:25], v[24:25], 0, s[18:19]
	s_nop 0
	v_lshlrev_b32_e32 v28, 16, v30
	v_and_b32_e32 v29, 0xffff0000, v30
	s_nop 0
	v_lshlrev_b32_e32 v54, 16, v42
	v_and_b32_e32 v55, 0xffff0000, v42
	v_and_b32_e32 v30, 0xffff0000, v31
	v_lshlrev_b32_e32 v31, 16, v31
	v_and_b32_e32 v42, 0xffff0000, v43
	v_lshlrev_b32_e32 v43, 16, v43
	v_pk_mul_f32 v[60:61], v[28:29], v[28:29]
	v_pk_mul_f32 v[64:65], v[54:55], v[54:55]
	s_nop 0
	v_lshlrev_b32_e32 v19, 16, v40
	v_and_b32_e32 v39, 0xffff0000, v40
	v_lshlrev_b32_e32 v40, 16, v41
	v_and_b32_e32 v41, 0xffff0000, v41
	v_lshlrev_b32_e32 v56, 16, v44
	v_and_b32_e32 v57, 0xffff0000, v44
	v_lshlrev_b32_e32 v58, 16, v46
	v_and_b32_e32 v59, 0xffff0000, v46
	v_pk_mul_f32 v[62:63], v[30:31], v[30:31]
	v_pk_mul_f32 v[66:67], v[42:43], v[42:43]
	v_mul_f32_e32 v86, 0xbfb8aa3b, v40
	v_mul_f32_e32 v87, 0xbfb8aa3b, v41
	v_mov_b32_e32 v40, v64
	v_mov_b32_e32 v41, v60
	v_mov_b32_e32 v60, v65
	v_and_b32_e32 v44, 0xffff0000, v45
	v_lshlrev_b32_e32 v45, 16, v45
	v_and_b32_e32 v46, 0xffff0000, v47
	v_lshlrev_b32_e32 v47, 16, v47
	v_pk_mul_f32 v[68:69], v[56:57], v[56:57]
	v_pk_mul_f32 v[72:73], v[58:59], v[58:59]
	s_nop 0
	v_lshlrev_b32_e32 v76, 16, v48
	v_and_b32_e32 v77, 0xffff0000, v48
	v_lshlrev_b32_e32 v78, 16, v49
	v_and_b32_e32 v79, 0xffff0000, v49
	s_nop 0
	v_lshlrev_b32_e32 v80, 16, v50
	v_and_b32_e32 v50, 0xffff0000, v50
	v_lshlrev_b32_e32 v81, 16, v51
	v_and_b32_e32 v51, 0xffff0000, v51
	v_mov_b32_e32 v48, v67
	v_mov_b32_e32 v49, v63
	v_pk_add_f32 v[40:41], v[40:41], v[60:61]
	v_pk_mul_f32 v[70:71], v[44:45], v[44:45]
	v_pk_mul_f32 v[74:75], v[46:47], v[46:47]
	v_mov_b32_e32 v67, v62
	v_mul_f32_e32 v63, 0xbfb8aa3b, v77
	v_mul_f32_e32 v65, 0xbfb8aa3b, v79
	v_mul_f32_e32 v77, 0xbfb8aa3b, v50
	v_mul_f32_e32 v79, 0xbfb8aa3b, v51
	v_mov_b32_e32 v50, v72
	v_mov_b32_e32 v51, v68
	v_mov_b32_e32 v68, v73
	v_pk_add_f32 v[40:41], v[48:49], v[40:41]
	s_nop 0
	v_lshlrev_b32_e32 v82, 16, v52
	v_and_b32_e32 v83, 0xffff0000, v52
	v_lshlrev_b32_e32 v84, 16, v53
	v_and_b32_e32 v85, 0xffff0000, v53
	v_mov_b32_e32 v52, v75
	v_mov_b32_e32 v53, v71
	v_pk_add_f32 v[50:51], v[50:51], v[68:69]
	v_pk_add_f32 v[40:41], v[66:67], v[40:41]
	v_pk_add_f32 v[48:49], v[52:53], v[50:51]
	ds_bpermute_b32 v51, v1, v41
	ds_bpermute_b32 v50, v1, v40
	v_mov_b32_e32 v75, v70
	v_pk_add_f32 v[48:49], v[74:75], v[48:49]
	ds_bpermute_b32 v53, v1, v49
	ds_bpermute_b32 v52, v1, v48
	s_waitcnt lgkmcnt(2)
	v_pk_add_f32 v[40:41], v[40:41], v[50:51]
	ds_bpermute_b32 v51, v34, v41
	ds_bpermute_b32 v50, v34, v40
	v_mul_f32_e32 v19, 0xbfb8aa3b, v19
	s_waitcnt lgkmcnt(2)
	v_pk_add_f32 v[48:49], v[48:49], v[52:53]
	ds_bpermute_b32 v53, v34, v49
	ds_bpermute_b32 v52, v34, v48
	s_waitcnt lgkmcnt(2)
	v_pk_add_f32 v[40:41], v[40:41], v[50:51]
	ds_bpermute_b32 v51, v35, v41
	ds_bpermute_b32 v50, v35, v40
	v_mul_f32_e32 v39, 0xbfb8aa3b, v39
	s_waitcnt lgkmcnt(2)
	v_pk_add_f32 v[48:49], v[48:49], v[52:53]
	ds_bpermute_b32 v53, v35, v49
	ds_bpermute_b32 v52, v35, v48
	s_waitcnt lgkmcnt(2)
	v_pk_add_f32 v[40:41], v[40:41], v[50:51]
	ds_bpermute_b32 v51, v36, v41
	ds_bpermute_b32 v50, v36, v40
	v_mul_f32_e32 v62, 0xbfb8aa3b, v76
	s_waitcnt lgkmcnt(2)
	v_pk_add_f32 v[48:49], v[48:49], v[52:53]
	ds_bpermute_b32 v53, v36, v49
	ds_bpermute_b32 v52, v36, v48
	s_waitcnt lgkmcnt(2)
	v_pk_add_f32 v[40:41], v[40:41], v[50:51]
	ds_bpermute_b32 v51, v37, v41
	ds_bpermute_b32 v50, v37, v40
	v_mul_f32_e32 v76, 0xbfb8aa3b, v80
	s_waitcnt lgkmcnt(2)
	v_pk_add_f32 v[48:49], v[48:49], v[52:53]
	ds_bpermute_b32 v53, v37, v49
	ds_bpermute_b32 v52, v37, v48
	s_waitcnt lgkmcnt(2)
	v_pk_add_f32 v[40:41], v[40:41], v[50:51]
	ds_bpermute_b32 v51, v38, v41
	ds_bpermute_b32 v50, v38, v40
	v_exp_f32_e32 v19, v19
	s_waitcnt lgkmcnt(2)
	v_pk_add_f32 v[48:49], v[48:49], v[52:53]
	ds_bpermute_b32 v53, v38, v49
	ds_bpermute_b32 v52, v38, v48
	s_waitcnt lgkmcnt(2)
	v_pk_add_f32 v[40:41], v[40:41], v[50:51]
	v_exp_f32_e32 v39, v39
	v_pk_fma_f32 v[40:41], v[40:41], s[22:23], v[26:27] op_sel_hi:[1,0,0]
	v_exp_f32_e32 v80, v86
	v_mul_f32_e32 v50, 0x4b800000, v41
	v_cmp_gt_f32_e64 s[8:9], s15, v41
	s_waitcnt lgkmcnt(0)
	v_pk_add_f32 v[48:49], v[48:49], v[52:53]
	v_mul_f32_e32 v64, 0xbfb8aa3b, v78
	v_cndmask_b32_e64 v41, v41, v50, s[8:9]
	v_mul_f32_e32 v78, 0xbfb8aa3b, v81
	v_exp_f32_e32 v81, v87
	v_pk_fma_f32 v[48:49], v[48:49], s[22:23], v[26:27] op_sel_hi:[1,0,0]
	v_mul_f32_e32 v51, 0x4b800000, v40
	v_cmp_gt_f32_e32 vcc, s15, v40
	v_rsq_f32_e32 v41, v41
	v_exp_f32_e32 v60, v62
	v_exp_f32_e32 v61, v63
	v_exp_f32_e32 v62, v64
	v_exp_f32_e32 v63, v65
	v_mul_f32_e32 v52, 0x4b800000, v49
	v_mul_f32_e32 v53, 0x4b800000, v48
	v_cmp_gt_f32_e64 s[4:5], s15, v48
	v_cmp_gt_f32_e64 s[6:7], s15, v49
	v_cndmask_b32_e32 v40, v40, v51, vcc
	v_mul_f32_e32 v70, 0xbfb8aa3b, v82
	v_mul_f32_e32 v71, 0xbfb8aa3b, v83
	v_mul_f32_e32 v72, 0xbfb8aa3b, v84
	v_mul_f32_e32 v73, 0xbfb8aa3b, v85
	v_exp_f32_e32 v64, v76
	v_exp_f32_e32 v65, v77
	v_exp_f32_e32 v76, v78
	v_exp_f32_e32 v77, v79
	v_cndmask_b32_e64 v49, v49, v52, s[6:7]
	v_cndmask_b32_e64 v48, v48, v53, s[4:5]
	v_rsq_f32_e32 v40, v40
	v_exp_f32_e32 v68, v70
	v_exp_f32_e32 v69, v71
	v_exp_f32_e32 v70, v72
	v_exp_f32_e32 v71, v73
	v_add_f32_e32 v19, 1.0, v19
	v_add_f32_e32 v39, 1.0, v39
	v_add_f32_e32 v66, 1.0, v80
	v_rsq_f32_e32 v49, v49
	v_rsq_f32_e32 v48, v48
	v_add_f32_e32 v67, 1.0, v81
	v_rcp_f32_e32 v19, v19
	v_rcp_f32_e32 v39, v39
	v_rcp_f32_e32 v66, v66
	v_mul_f32_e32 v50, 0x45800000, v41
	v_add_f32_e32 v60, 1.0, v60
	v_add_f32_e32 v61, 1.0, v61
	v_add_f32_e32 v62, 1.0, v62
	v_add_f32_e32 v63, 1.0, v63
	v_rcp_f32_e32 v67, v67
	v_cndmask_b32_e64 v41, v41, v50, s[8:9]
	v_add_f32_e32 v64, 1.0, v64
	v_add_f32_e32 v65, 1.0, v65
	v_add_f32_e32 v72, 1.0, v76
	v_add_f32_e32 v73, 1.0, v77
	v_rcp_f32_e32 v60, v60
	v_rcp_f32_e32 v61, v61
	v_rcp_f32_e32 v62, v62
	v_rcp_f32_e32 v63, v63
	v_mul_f32_e32 v51, 0x45800000, v40
	v_mul_f32_e32 v28, v41, v28
	v_mul_f32_e32 v29, v41, v29
	v_mul_f32_e32 v31, v41, v31
	v_add_f32_e32 v68, 1.0, v68
	v_add_f32_e32 v69, 1.0, v69
	v_add_f32_e32 v70, 1.0, v70
	v_add_f32_e32 v71, 1.0, v71
	v_rcp_f32_e32 v64, v64
	v_rcp_f32_e32 v65, v65
	v_rcp_f32_e32 v72, v72
	v_rcp_f32_e32 v73, v73
	v_mul_f32_e32 v52, 0x45800000, v49
	v_mul_f32_e32 v53, 0x45800000, v48
	v_cndmask_b32_e32 v40, v40, v51, vcc
	v_mul_f32_e32 v30, v41, v30
	v_mul_f32_e32 v28, v14, v28
	v_mul_f32_e32 v29, v15, v29
	v_mul_f32_e32 v31, v16, v31
	v_rcp_f32_e32 v68, v68
	v_rcp_f32_e32 v69, v69
	v_rcp_f32_e32 v70, v70
	v_rcp_f32_e32 v71, v71
	v_cndmask_b32_e64 v49, v49, v52, s[6:7]
	v_cndmask_b32_e64 v48, v48, v53, s[4:5]
	v_mul_f32_e32 v41, v40, v54
	v_mul_f32_e32 v50, v40, v55
	v_mul_f32_e32 v43, v40, v43
	v_mul_f32_e32 v40, v40, v42
	v_mul_f32_e32 v30, v17, v30
	v_mul_f32_e32 v19, v19, v28
	v_mul_f32_e32 v28, v39, v29
	v_mul_f32_e32 v29, v66, v31
	v_mul_f32_e32 v42, v49, v56
	v_mul_f32_e32 v51, v49, v57
	v_mul_f32_e32 v45, v49, v45
	v_mul_f32_e32 v44, v49, v44
	v_mul_f32_e32 v49, v48, v58
	v_mul_f32_e32 v52, v48, v59
	v_mul_f32_e32 v47, v48, v47
	v_mul_f32_e32 v46, v48, v46
	v_mul_f32_e32 v41, v10, v41
	v_mul_f32_e32 v48, v11, v50
	v_mul_f32_e32 v43, v12, v43
	v_mul_f32_e32 v40, v13, v40
	v_mul_f32_e32 v30, v67, v30
	v_cvt_pk_bf16_f32 v28, v19, v28
	v_cvt_pk_bf16_f32 v29, v29, v30
	v_mul_f32_e32 v42, v6, v42
	v_mul_f32_e32 v50, v7, v51
	v_mul_f32_e32 v45, v8, v45
	v_mul_f32_e32 v44, v9, v44
	v_mul_f32_e32 v31, v60, v41
	v_mul_f32_e32 v39, v61, v48
	v_mul_f32_e32 v41, v62, v43
	v_mul_f32_e32 v40, v63, v40
	global_store_dwordx2 v[32:33], v[28:29], off
	v_cvt_pk_bf16_f32 v28, v31, v39
	v_cvt_pk_bf16_f32 v29, v41, v40
	v_mul_f32_e32 v49, v2, v49
	v_mul_f32_e32 v51, v3, v52
	v_mul_f32_e32 v47, v4, v47
	v_mul_f32_e32 v46, v5, v46
	v_mul_f32_e32 v42, v64, v42
	v_mul_f32_e32 v43, v65, v50
	v_mul_f32_e32 v45, v72, v45
	v_mul_f32_e32 v44, v73, v44
	global_store_dwordx2 v[32:33], v[28:29], off offset:512
	v_cvt_pk_bf16_f32 v28, v42, v43
	v_cvt_pk_bf16_f32 v29, v45, v44
	v_mul_f32_e32 v48, v68, v49
	v_mul_f32_e32 v49, v69, v51
	v_mul_f32_e32 v47, v70, v47
	v_mul_f32_e32 v46, v71, v46
	global_store_dwordx2 v[32:33], v[28:29], off offset:1024
	v_cvt_pk_bf16_f32 v28, v48, v49
	v_cvt_pk_bf16_f32 v29, v47, v46
	global_store_dwordx2 v[32:33], v[28:29], off offset:1536
	s_andn2_b64 exec, exec, s[20:21]
	s_nop 0
	v_lshl_add_u64 v[30:31], v[24:25], 0, v[20:21]
	v_add_co_u32_e32 v40, vcc, 0x3ec4a000, v30
	v_lshl_add_u64 v[28:29], v[22:23], 0, v[20:21]
	v_add_co_u32_e64 v32, s[4:5], s23, v30
	v_addc_co_u32_e32 v41, vcc, 0, v31, vcc
	s_nop 0
	v_addc_co_u32_e64 v33, s[4:5], 0, v31, s[4:5]
	v_add_co_u32_e32 v28, vcc, 0x42c4b000, v28
	s_waitcnt vmcnt(36)
	v_mov_b32_e32 v30, v176
	v_mov_b32_e32 v31, v177
	v_mov_b32_e32 v42, v178
	v_mov_b32_e32 v43, v179
	v_mov_b32_e32 v44, v180
	v_mov_b32_e32 v45, v181
	v_mov_b32_e32 v46, v182
	v_mov_b32_e32 v47, v183
	v_mov_b32_e32 v40, v184
	v_mov_b32_e32 v41, v185
	v_mov_b32_e32 v48, v186
	v_mov_b32_e32 v49, v187
	v_mov_b32_e32 v50, v188
	v_mov_b32_e32 v51, v189
	v_mov_b32_e32 v52, v190
	v_mov_b32_e32 v53, v191
	v_addc_co_u32_e32 v29, vcc, 0, v29, vcc
	v_add_u32_e32 v18, s14, v18
	v_cmp_lt_i32_e64 s[4:5], s24, v18
	s_or_b64 s[20:21], s[4:5], s[20:21]
	v_lshl_add_u64 v[22:23], v[22:23], 0, s[16:17]
	v_lshl_add_u64 v[24:25], v[24:25], 0, s[18:19]
	s_nop 0
	v_lshlrev_b32_e32 v28, 16, v30
	v_and_b32_e32 v29, 0xffff0000, v30
	s_nop 0
	v_lshlrev_b32_e32 v54, 16, v42
	v_and_b32_e32 v55, 0xffff0000, v42
	v_and_b32_e32 v30, 0xffff0000, v31
	v_lshlrev_b32_e32 v31, 16, v31
	v_and_b32_e32 v42, 0xffff0000, v43
	v_lshlrev_b32_e32 v43, 16, v43
	v_pk_mul_f32 v[60:61], v[28:29], v[28:29]
	v_pk_mul_f32 v[64:65], v[54:55], v[54:55]
	s_nop 0
	v_lshlrev_b32_e32 v19, 16, v40
	v_and_b32_e32 v39, 0xffff0000, v40
	v_lshlrev_b32_e32 v40, 16, v41
	v_and_b32_e32 v41, 0xffff0000, v41
	v_lshlrev_b32_e32 v56, 16, v44
	v_and_b32_e32 v57, 0xffff0000, v44
	v_lshlrev_b32_e32 v58, 16, v46
	v_and_b32_e32 v59, 0xffff0000, v46
	v_pk_mul_f32 v[62:63], v[30:31], v[30:31]
	v_pk_mul_f32 v[66:67], v[42:43], v[42:43]
	v_mul_f32_e32 v86, 0xbfb8aa3b, v40
	v_mul_f32_e32 v87, 0xbfb8aa3b, v41
	v_mov_b32_e32 v40, v64
	v_mov_b32_e32 v41, v60
	v_mov_b32_e32 v60, v65
	v_and_b32_e32 v44, 0xffff0000, v45
	v_lshlrev_b32_e32 v45, 16, v45
	v_and_b32_e32 v46, 0xffff0000, v47
	v_lshlrev_b32_e32 v47, 16, v47
	v_pk_mul_f32 v[68:69], v[56:57], v[56:57]
	v_pk_mul_f32 v[72:73], v[58:59], v[58:59]
	s_nop 0
	v_lshlrev_b32_e32 v76, 16, v48
	v_and_b32_e32 v77, 0xffff0000, v48
	v_lshlrev_b32_e32 v78, 16, v49
	v_and_b32_e32 v79, 0xffff0000, v49
	s_nop 0
	v_lshlrev_b32_e32 v80, 16, v50
	v_and_b32_e32 v50, 0xffff0000, v50
	v_lshlrev_b32_e32 v81, 16, v51
	v_and_b32_e32 v51, 0xffff0000, v51
	v_mov_b32_e32 v48, v67
	v_mov_b32_e32 v49, v63
	v_pk_add_f32 v[40:41], v[40:41], v[60:61]
	v_pk_mul_f32 v[70:71], v[44:45], v[44:45]
	v_pk_mul_f32 v[74:75], v[46:47], v[46:47]
	v_mov_b32_e32 v67, v62
	v_mul_f32_e32 v63, 0xbfb8aa3b, v77
	v_mul_f32_e32 v65, 0xbfb8aa3b, v79
	v_mul_f32_e32 v77, 0xbfb8aa3b, v50
	v_mul_f32_e32 v79, 0xbfb8aa3b, v51
	v_mov_b32_e32 v50, v72
	v_mov_b32_e32 v51, v68
	v_mov_b32_e32 v68, v73
	v_pk_add_f32 v[40:41], v[48:49], v[40:41]
	s_nop 0
	v_lshlrev_b32_e32 v82, 16, v52
	v_and_b32_e32 v83, 0xffff0000, v52
	v_lshlrev_b32_e32 v84, 16, v53
	v_and_b32_e32 v85, 0xffff0000, v53
	v_mov_b32_e32 v52, v75
	v_mov_b32_e32 v53, v71
	v_pk_add_f32 v[50:51], v[50:51], v[68:69]
	v_pk_add_f32 v[40:41], v[66:67], v[40:41]
	v_pk_add_f32 v[48:49], v[52:53], v[50:51]
	ds_bpermute_b32 v51, v1, v41
	ds_bpermute_b32 v50, v1, v40
	v_mov_b32_e32 v75, v70
	v_pk_add_f32 v[48:49], v[74:75], v[48:49]
	ds_bpermute_b32 v53, v1, v49
	ds_bpermute_b32 v52, v1, v48
	s_waitcnt lgkmcnt(2)
	v_pk_add_f32 v[40:41], v[40:41], v[50:51]
	ds_bpermute_b32 v51, v34, v41
	ds_bpermute_b32 v50, v34, v40
	v_mul_f32_e32 v19, 0xbfb8aa3b, v19
	s_waitcnt lgkmcnt(2)
	v_pk_add_f32 v[48:49], v[48:49], v[52:53]
	ds_bpermute_b32 v53, v34, v49
	ds_bpermute_b32 v52, v34, v48
	s_waitcnt lgkmcnt(2)
	v_pk_add_f32 v[40:41], v[40:41], v[50:51]
	ds_bpermute_b32 v51, v35, v41
	ds_bpermute_b32 v50, v35, v40
	v_mul_f32_e32 v39, 0xbfb8aa3b, v39
	s_waitcnt lgkmcnt(2)
	v_pk_add_f32 v[48:49], v[48:49], v[52:53]
	ds_bpermute_b32 v53, v35, v49
	ds_bpermute_b32 v52, v35, v48
	s_waitcnt lgkmcnt(2)
	v_pk_add_f32 v[40:41], v[40:41], v[50:51]
	ds_bpermute_b32 v51, v36, v41
	ds_bpermute_b32 v50, v36, v40
	v_mul_f32_e32 v62, 0xbfb8aa3b, v76
	s_waitcnt lgkmcnt(2)
	v_pk_add_f32 v[48:49], v[48:49], v[52:53]
	ds_bpermute_b32 v53, v36, v49
	ds_bpermute_b32 v52, v36, v48
	s_waitcnt lgkmcnt(2)
	v_pk_add_f32 v[40:41], v[40:41], v[50:51]
	ds_bpermute_b32 v51, v37, v41
	ds_bpermute_b32 v50, v37, v40
	v_mul_f32_e32 v76, 0xbfb8aa3b, v80
	s_waitcnt lgkmcnt(2)
	v_pk_add_f32 v[48:49], v[48:49], v[52:53]
	ds_bpermute_b32 v53, v37, v49
	ds_bpermute_b32 v52, v37, v48
	s_waitcnt lgkmcnt(2)
	v_pk_add_f32 v[40:41], v[40:41], v[50:51]
	ds_bpermute_b32 v51, v38, v41
	ds_bpermute_b32 v50, v38, v40
	v_exp_f32_e32 v19, v19
	s_waitcnt lgkmcnt(2)
	v_pk_add_f32 v[48:49], v[48:49], v[52:53]
	ds_bpermute_b32 v53, v38, v49
	ds_bpermute_b32 v52, v38, v48
	s_waitcnt lgkmcnt(2)
	v_pk_add_f32 v[40:41], v[40:41], v[50:51]
	v_exp_f32_e32 v39, v39
	v_pk_fma_f32 v[40:41], v[40:41], s[22:23], v[26:27] op_sel_hi:[1,0,0]
	v_exp_f32_e32 v80, v86
	v_mul_f32_e32 v50, 0x4b800000, v41
	v_cmp_gt_f32_e64 s[8:9], s15, v41
	s_waitcnt lgkmcnt(0)
	v_pk_add_f32 v[48:49], v[48:49], v[52:53]
	v_mul_f32_e32 v64, 0xbfb8aa3b, v78
	v_cndmask_b32_e64 v41, v41, v50, s[8:9]
	v_mul_f32_e32 v78, 0xbfb8aa3b, v81
	v_exp_f32_e32 v81, v87
	v_pk_fma_f32 v[48:49], v[48:49], s[22:23], v[26:27] op_sel_hi:[1,0,0]
	v_mul_f32_e32 v51, 0x4b800000, v40
	v_cmp_gt_f32_e32 vcc, s15, v40
	v_rsq_f32_e32 v41, v41
	v_exp_f32_e32 v60, v62
	v_exp_f32_e32 v61, v63
	v_exp_f32_e32 v62, v64
	v_exp_f32_e32 v63, v65
	v_mul_f32_e32 v52, 0x4b800000, v49
	v_mul_f32_e32 v53, 0x4b800000, v48
	v_cmp_gt_f32_e64 s[4:5], s15, v48
	v_cmp_gt_f32_e64 s[6:7], s15, v49
	v_cndmask_b32_e32 v40, v40, v51, vcc
	v_mul_f32_e32 v70, 0xbfb8aa3b, v82
	v_mul_f32_e32 v71, 0xbfb8aa3b, v83
	v_mul_f32_e32 v72, 0xbfb8aa3b, v84
	v_mul_f32_e32 v73, 0xbfb8aa3b, v85
	v_exp_f32_e32 v64, v76
	v_exp_f32_e32 v65, v77
	v_exp_f32_e32 v76, v78
	v_exp_f32_e32 v77, v79
	v_cndmask_b32_e64 v49, v49, v52, s[6:7]
	v_cndmask_b32_e64 v48, v48, v53, s[4:5]
	v_rsq_f32_e32 v40, v40
	v_exp_f32_e32 v68, v70
	v_exp_f32_e32 v69, v71
	v_exp_f32_e32 v70, v72
	v_exp_f32_e32 v71, v73
	v_add_f32_e32 v19, 1.0, v19
	v_add_f32_e32 v39, 1.0, v39
	v_add_f32_e32 v66, 1.0, v80
	v_rsq_f32_e32 v49, v49
	v_rsq_f32_e32 v48, v48
	v_add_f32_e32 v67, 1.0, v81
	v_rcp_f32_e32 v19, v19
	v_rcp_f32_e32 v39, v39
	v_rcp_f32_e32 v66, v66
	v_mul_f32_e32 v50, 0x45800000, v41
	v_add_f32_e32 v60, 1.0, v60
	v_add_f32_e32 v61, 1.0, v61
	v_add_f32_e32 v62, 1.0, v62
	v_add_f32_e32 v63, 1.0, v63
	v_rcp_f32_e32 v67, v67
	v_cndmask_b32_e64 v41, v41, v50, s[8:9]
	v_add_f32_e32 v64, 1.0, v64
	v_add_f32_e32 v65, 1.0, v65
	v_add_f32_e32 v72, 1.0, v76
	v_add_f32_e32 v73, 1.0, v77
	v_rcp_f32_e32 v60, v60
	v_rcp_f32_e32 v61, v61
	v_rcp_f32_e32 v62, v62
	v_rcp_f32_e32 v63, v63
	v_mul_f32_e32 v51, 0x45800000, v40
	v_mul_f32_e32 v28, v41, v28
	v_mul_f32_e32 v29, v41, v29
	v_mul_f32_e32 v31, v41, v31
	v_add_f32_e32 v68, 1.0, v68
	v_add_f32_e32 v69, 1.0, v69
	v_add_f32_e32 v70, 1.0, v70
	v_add_f32_e32 v71, 1.0, v71
	v_rcp_f32_e32 v64, v64
	v_rcp_f32_e32 v65, v65
	v_rcp_f32_e32 v72, v72
	v_rcp_f32_e32 v73, v73
	v_mul_f32_e32 v52, 0x45800000, v49
	v_mul_f32_e32 v53, 0x45800000, v48
	v_cndmask_b32_e32 v40, v40, v51, vcc
	v_mul_f32_e32 v30, v41, v30
	v_mul_f32_e32 v28, v14, v28
	v_mul_f32_e32 v29, v15, v29
	v_mul_f32_e32 v31, v16, v31
	v_rcp_f32_e32 v68, v68
	v_rcp_f32_e32 v69, v69
	v_rcp_f32_e32 v70, v70
	v_rcp_f32_e32 v71, v71
	v_cndmask_b32_e64 v49, v49, v52, s[6:7]
	v_cndmask_b32_e64 v48, v48, v53, s[4:5]
	v_mul_f32_e32 v41, v40, v54
	v_mul_f32_e32 v50, v40, v55
	v_mul_f32_e32 v43, v40, v43
	v_mul_f32_e32 v40, v40, v42
	v_mul_f32_e32 v30, v17, v30
	v_mul_f32_e32 v19, v19, v28
	v_mul_f32_e32 v28, v39, v29
	v_mul_f32_e32 v29, v66, v31
	v_mul_f32_e32 v42, v49, v56
	v_mul_f32_e32 v51, v49, v57
	v_mul_f32_e32 v45, v49, v45
	v_mul_f32_e32 v44, v49, v44
	v_mul_f32_e32 v49, v48, v58
	v_mul_f32_e32 v52, v48, v59
	v_mul_f32_e32 v47, v48, v47
	v_mul_f32_e32 v46, v48, v46
	v_mul_f32_e32 v41, v10, v41
	v_mul_f32_e32 v48, v11, v50
	v_mul_f32_e32 v43, v12, v43
	v_mul_f32_e32 v40, v13, v40
	v_mul_f32_e32 v30, v67, v30
	v_cvt_pk_bf16_f32 v28, v19, v28
	v_cvt_pk_bf16_f32 v29, v29, v30
	v_mul_f32_e32 v42, v6, v42
	v_mul_f32_e32 v50, v7, v51
	v_mul_f32_e32 v45, v8, v45
	v_mul_f32_e32 v44, v9, v44
	v_mul_f32_e32 v31, v60, v41
	v_mul_f32_e32 v39, v61, v48
	v_mul_f32_e32 v41, v62, v43
	v_mul_f32_e32 v40, v63, v40
	global_store_dwordx2 v[32:33], v[28:29], off
	v_cvt_pk_bf16_f32 v28, v31, v39
	v_cvt_pk_bf16_f32 v29, v41, v40
	v_mul_f32_e32 v49, v2, v49
	v_mul_f32_e32 v51, v3, v52
	v_mul_f32_e32 v47, v4, v47
	v_mul_f32_e32 v46, v5, v46
	v_mul_f32_e32 v42, v64, v42
	v_mul_f32_e32 v43, v65, v50
	v_mul_f32_e32 v45, v72, v45
	v_mul_f32_e32 v44, v73, v44
	global_store_dwordx2 v[32:33], v[28:29], off offset:512
	v_cvt_pk_bf16_f32 v28, v42, v43
	v_cvt_pk_bf16_f32 v29, v45, v44
	v_mul_f32_e32 v48, v68, v49
	v_mul_f32_e32 v49, v69, v51
	v_mul_f32_e32 v47, v70, v47
	v_mul_f32_e32 v46, v71, v46
	global_store_dwordx2 v[32:33], v[28:29], off offset:1024
	v_cvt_pk_bf16_f32 v28, v48, v49
	v_cvt_pk_bf16_f32 v29, v47, v46
	global_store_dwordx2 v[32:33], v[28:29], off offset:1536
	s_andn2_b64 exec, exec, s[20:21]
	s_nop 0
	v_lshl_add_u64 v[30:31], v[24:25], 0, v[20:21]
	v_add_co_u32_e32 v40, vcc, 0x3ec4a000, v30
	v_lshl_add_u64 v[28:29], v[22:23], 0, v[20:21]
	v_add_co_u32_e64 v32, s[4:5], s23, v30
	v_addc_co_u32_e32 v41, vcc, 0, v31, vcc
	s_nop 0
	v_addc_co_u32_e64 v33, s[4:5], 0, v31, s[4:5]
	v_add_co_u32_e32 v28, vcc, 0x42c4b000, v28
	s_waitcnt vmcnt(32)
	v_mov_b32_e32 v30, v192
	v_mov_b32_e32 v31, v193
	v_mov_b32_e32 v42, v194
	v_mov_b32_e32 v43, v195
	v_mov_b32_e32 v44, v196
	v_mov_b32_e32 v45, v197
	v_mov_b32_e32 v46, v198
	v_mov_b32_e32 v47, v199
	v_mov_b32_e32 v40, v200
	v_mov_b32_e32 v41, v201
	v_mov_b32_e32 v48, v202
	v_mov_b32_e32 v49, v203
	v_mov_b32_e32 v50, v204
	v_mov_b32_e32 v51, v205
	v_mov_b32_e32 v52, v206
	v_mov_b32_e32 v53, v207
	v_addc_co_u32_e32 v29, vcc, 0, v29, vcc
	v_add_u32_e32 v18, s14, v18
	v_cmp_lt_i32_e64 s[4:5], s24, v18
	s_or_b64 s[20:21], s[4:5], s[20:21]
	v_lshl_add_u64 v[22:23], v[22:23], 0, s[16:17]
	v_lshl_add_u64 v[24:25], v[24:25], 0, s[18:19]
	s_nop 0
	v_lshlrev_b32_e32 v28, 16, v30
	v_and_b32_e32 v29, 0xffff0000, v30
	s_nop 0
	v_lshlrev_b32_e32 v54, 16, v42
	v_and_b32_e32 v55, 0xffff0000, v42
	v_and_b32_e32 v30, 0xffff0000, v31
	v_lshlrev_b32_e32 v31, 16, v31
	v_and_b32_e32 v42, 0xffff0000, v43
	v_lshlrev_b32_e32 v43, 16, v43
	v_pk_mul_f32 v[60:61], v[28:29], v[28:29]
	v_pk_mul_f32 v[64:65], v[54:55], v[54:55]
	s_nop 0
	v_lshlrev_b32_e32 v19, 16, v40
	v_and_b32_e32 v39, 0xffff0000, v40
	v_lshlrev_b32_e32 v40, 16, v41
	v_and_b32_e32 v41, 0xffff0000, v41
	v_lshlrev_b32_e32 v56, 16, v44
	v_and_b32_e32 v57, 0xffff0000, v44
	v_lshlrev_b32_e32 v58, 16, v46
	v_and_b32_e32 v59, 0xffff0000, v46
	v_pk_mul_f32 v[62:63], v[30:31], v[30:31]
	v_pk_mul_f32 v[66:67], v[42:43], v[42:43]
	v_mul_f32_e32 v86, 0xbfb8aa3b, v40
	v_mul_f32_e32 v87, 0xbfb8aa3b, v41
	v_mov_b32_e32 v40, v64
	v_mov_b32_e32 v41, v60
	v_mov_b32_e32 v60, v65
	v_and_b32_e32 v44, 0xffff0000, v45
	v_lshlrev_b32_e32 v45, 16, v45
	v_and_b32_e32 v46, 0xffff0000, v47
	v_lshlrev_b32_e32 v47, 16, v47
	v_pk_mul_f32 v[68:69], v[56:57], v[56:57]
	v_pk_mul_f32 v[72:73], v[58:59], v[58:59]
	s_nop 0
	v_lshlrev_b32_e32 v76, 16, v48
	v_and_b32_e32 v77, 0xffff0000, v48
	v_lshlrev_b32_e32 v78, 16, v49
	v_and_b32_e32 v79, 0xffff0000, v49
	s_nop 0
	v_lshlrev_b32_e32 v80, 16, v50
	v_and_b32_e32 v50, 0xffff0000, v50
	v_lshlrev_b32_e32 v81, 16, v51
	v_and_b32_e32 v51, 0xffff0000, v51
	v_mov_b32_e32 v48, v67
	v_mov_b32_e32 v49, v63
	v_pk_add_f32 v[40:41], v[40:41], v[60:61]
	v_pk_mul_f32 v[70:71], v[44:45], v[44:45]
	v_pk_mul_f32 v[74:75], v[46:47], v[46:47]
	v_mov_b32_e32 v67, v62
	v_mul_f32_e32 v63, 0xbfb8aa3b, v77
	v_mul_f32_e32 v65, 0xbfb8aa3b, v79
	v_mul_f32_e32 v77, 0xbfb8aa3b, v50
	v_mul_f32_e32 v79, 0xbfb8aa3b, v51
	v_mov_b32_e32 v50, v72
	v_mov_b32_e32 v51, v68
	v_mov_b32_e32 v68, v73
	v_pk_add_f32 v[40:41], v[48:49], v[40:41]
	s_nop 0
	v_lshlrev_b32_e32 v82, 16, v52
	v_and_b32_e32 v83, 0xffff0000, v52
	v_lshlrev_b32_e32 v84, 16, v53
	v_and_b32_e32 v85, 0xffff0000, v53
	v_mov_b32_e32 v52, v75
	v_mov_b32_e32 v53, v71
	v_pk_add_f32 v[50:51], v[50:51], v[68:69]
	v_pk_add_f32 v[40:41], v[66:67], v[40:41]
	v_pk_add_f32 v[48:49], v[52:53], v[50:51]
	ds_bpermute_b32 v51, v1, v41
	ds_bpermute_b32 v50, v1, v40
	v_mov_b32_e32 v75, v70
	v_pk_add_f32 v[48:49], v[74:75], v[48:49]
	ds_bpermute_b32 v53, v1, v49
	ds_bpermute_b32 v52, v1, v48
	s_waitcnt lgkmcnt(2)
	v_pk_add_f32 v[40:41], v[40:41], v[50:51]
	ds_bpermute_b32 v51, v34, v41
	ds_bpermute_b32 v50, v34, v40
	v_mul_f32_e32 v19, 0xbfb8aa3b, v19
	s_waitcnt lgkmcnt(2)
	v_pk_add_f32 v[48:49], v[48:49], v[52:53]
	ds_bpermute_b32 v53, v34, v49
	ds_bpermute_b32 v52, v34, v48
	s_waitcnt lgkmcnt(2)
	v_pk_add_f32 v[40:41], v[40:41], v[50:51]
	ds_bpermute_b32 v51, v35, v41
	ds_bpermute_b32 v50, v35, v40
	v_mul_f32_e32 v39, 0xbfb8aa3b, v39
	s_waitcnt lgkmcnt(2)
	v_pk_add_f32 v[48:49], v[48:49], v[52:53]
	ds_bpermute_b32 v53, v35, v49
	ds_bpermute_b32 v52, v35, v48
	s_waitcnt lgkmcnt(2)
	v_pk_add_f32 v[40:41], v[40:41], v[50:51]
	ds_bpermute_b32 v51, v36, v41
	ds_bpermute_b32 v50, v36, v40
	v_mul_f32_e32 v62, 0xbfb8aa3b, v76
	s_waitcnt lgkmcnt(2)
	v_pk_add_f32 v[48:49], v[48:49], v[52:53]
	ds_bpermute_b32 v53, v36, v49
	ds_bpermute_b32 v52, v36, v48
	s_waitcnt lgkmcnt(2)
	v_pk_add_f32 v[40:41], v[40:41], v[50:51]
	ds_bpermute_b32 v51, v37, v41
	ds_bpermute_b32 v50, v37, v40
	v_mul_f32_e32 v76, 0xbfb8aa3b, v80
	s_waitcnt lgkmcnt(2)
	v_pk_add_f32 v[48:49], v[48:49], v[52:53]
	ds_bpermute_b32 v53, v37, v49
	ds_bpermute_b32 v52, v37, v48
	s_waitcnt lgkmcnt(2)
	v_pk_add_f32 v[40:41], v[40:41], v[50:51]
	ds_bpermute_b32 v51, v38, v41
	ds_bpermute_b32 v50, v38, v40
	v_exp_f32_e32 v19, v19
	s_waitcnt lgkmcnt(2)
	v_pk_add_f32 v[48:49], v[48:49], v[52:53]
	ds_bpermute_b32 v53, v38, v49
	ds_bpermute_b32 v52, v38, v48
	s_waitcnt lgkmcnt(2)
	v_pk_add_f32 v[40:41], v[40:41], v[50:51]
	v_exp_f32_e32 v39, v39
	v_pk_fma_f32 v[40:41], v[40:41], s[22:23], v[26:27] op_sel_hi:[1,0,0]
	v_exp_f32_e32 v80, v86
	v_mul_f32_e32 v50, 0x4b800000, v41
	v_cmp_gt_f32_e64 s[8:9], s15, v41
	s_waitcnt lgkmcnt(0)
	v_pk_add_f32 v[48:49], v[48:49], v[52:53]
	v_mul_f32_e32 v64, 0xbfb8aa3b, v78
	v_cndmask_b32_e64 v41, v41, v50, s[8:9]
	v_mul_f32_e32 v78, 0xbfb8aa3b, v81
	v_exp_f32_e32 v81, v87
	v_pk_fma_f32 v[48:49], v[48:49], s[22:23], v[26:27] op_sel_hi:[1,0,0]
	v_mul_f32_e32 v51, 0x4b800000, v40
	v_cmp_gt_f32_e32 vcc, s15, v40
	v_rsq_f32_e32 v41, v41
	v_exp_f32_e32 v60, v62
	v_exp_f32_e32 v61, v63
	v_exp_f32_e32 v62, v64
	v_exp_f32_e32 v63, v65
	v_mul_f32_e32 v52, 0x4b800000, v49
	v_mul_f32_e32 v53, 0x4b800000, v48
	v_cmp_gt_f32_e64 s[4:5], s15, v48
	v_cmp_gt_f32_e64 s[6:7], s15, v49
	v_cndmask_b32_e32 v40, v40, v51, vcc
	v_mul_f32_e32 v70, 0xbfb8aa3b, v82
	v_mul_f32_e32 v71, 0xbfb8aa3b, v83
	v_mul_f32_e32 v72, 0xbfb8aa3b, v84
	v_mul_f32_e32 v73, 0xbfb8aa3b, v85
	v_exp_f32_e32 v64, v76
	v_exp_f32_e32 v65, v77
	v_exp_f32_e32 v76, v78
	v_exp_f32_e32 v77, v79
	v_cndmask_b32_e64 v49, v49, v52, s[6:7]
	v_cndmask_b32_e64 v48, v48, v53, s[4:5]
	v_rsq_f32_e32 v40, v40
	v_exp_f32_e32 v68, v70
	v_exp_f32_e32 v69, v71
	v_exp_f32_e32 v70, v72
	v_exp_f32_e32 v71, v73
	v_add_f32_e32 v19, 1.0, v19
	v_add_f32_e32 v39, 1.0, v39
	v_add_f32_e32 v66, 1.0, v80
	v_rsq_f32_e32 v49, v49
	v_rsq_f32_e32 v48, v48
	v_add_f32_e32 v67, 1.0, v81
	v_rcp_f32_e32 v19, v19
	v_rcp_f32_e32 v39, v39
	v_rcp_f32_e32 v66, v66
	v_mul_f32_e32 v50, 0x45800000, v41
	v_add_f32_e32 v60, 1.0, v60
	v_add_f32_e32 v61, 1.0, v61
	v_add_f32_e32 v62, 1.0, v62
	v_add_f32_e32 v63, 1.0, v63
	v_rcp_f32_e32 v67, v67
	v_cndmask_b32_e64 v41, v41, v50, s[8:9]
	v_add_f32_e32 v64, 1.0, v64
	v_add_f32_e32 v65, 1.0, v65
	v_add_f32_e32 v72, 1.0, v76
	v_add_f32_e32 v73, 1.0, v77
	v_rcp_f32_e32 v60, v60
	v_rcp_f32_e32 v61, v61
	v_rcp_f32_e32 v62, v62
	v_rcp_f32_e32 v63, v63
	v_mul_f32_e32 v51, 0x45800000, v40
	v_mul_f32_e32 v28, v41, v28
	v_mul_f32_e32 v29, v41, v29
	v_mul_f32_e32 v31, v41, v31
	v_add_f32_e32 v68, 1.0, v68
	v_add_f32_e32 v69, 1.0, v69
	v_add_f32_e32 v70, 1.0, v70
	v_add_f32_e32 v71, 1.0, v71
	v_rcp_f32_e32 v64, v64
	v_rcp_f32_e32 v65, v65
	v_rcp_f32_e32 v72, v72
	v_rcp_f32_e32 v73, v73
	v_mul_f32_e32 v52, 0x45800000, v49
	v_mul_f32_e32 v53, 0x45800000, v48
	v_cndmask_b32_e32 v40, v40, v51, vcc
	v_mul_f32_e32 v30, v41, v30
	v_mul_f32_e32 v28, v14, v28
	v_mul_f32_e32 v29, v15, v29
	v_mul_f32_e32 v31, v16, v31
	v_rcp_f32_e32 v68, v68
	v_rcp_f32_e32 v69, v69
	v_rcp_f32_e32 v70, v70
	v_rcp_f32_e32 v71, v71
	v_cndmask_b32_e64 v49, v49, v52, s[6:7]
	v_cndmask_b32_e64 v48, v48, v53, s[4:5]
	v_mul_f32_e32 v41, v40, v54
	v_mul_f32_e32 v50, v40, v55
	v_mul_f32_e32 v43, v40, v43
	v_mul_f32_e32 v40, v40, v42
	v_mul_f32_e32 v30, v17, v30
	v_mul_f32_e32 v19, v19, v28
	v_mul_f32_e32 v28, v39, v29
	v_mul_f32_e32 v29, v66, v31
	v_mul_f32_e32 v42, v49, v56
	v_mul_f32_e32 v51, v49, v57
	v_mul_f32_e32 v45, v49, v45
	v_mul_f32_e32 v44, v49, v44
	v_mul_f32_e32 v49, v48, v58
	v_mul_f32_e32 v52, v48, v59
	v_mul_f32_e32 v47, v48, v47
	v_mul_f32_e32 v46, v48, v46
	v_mul_f32_e32 v41, v10, v41
	v_mul_f32_e32 v48, v11, v50
	v_mul_f32_e32 v43, v12, v43
	v_mul_f32_e32 v40, v13, v40
	v_mul_f32_e32 v30, v67, v30
	v_cvt_pk_bf16_f32 v28, v19, v28
	v_cvt_pk_bf16_f32 v29, v29, v30
	v_mul_f32_e32 v42, v6, v42
	v_mul_f32_e32 v50, v7, v51
	v_mul_f32_e32 v45, v8, v45
	v_mul_f32_e32 v44, v9, v44
	v_mul_f32_e32 v31, v60, v41
	v_mul_f32_e32 v39, v61, v48
	v_mul_f32_e32 v41, v62, v43
	v_mul_f32_e32 v40, v63, v40
	global_store_dwordx2 v[32:33], v[28:29], off
	v_cvt_pk_bf16_f32 v28, v31, v39
	v_cvt_pk_bf16_f32 v29, v41, v40
	v_mul_f32_e32 v49, v2, v49
	v_mul_f32_e32 v51, v3, v52
	v_mul_f32_e32 v47, v4, v47
	v_mul_f32_e32 v46, v5, v46
	v_mul_f32_e32 v42, v64, v42
	v_mul_f32_e32 v43, v65, v50
	v_mul_f32_e32 v45, v72, v45
	v_mul_f32_e32 v44, v73, v44
	global_store_dwordx2 v[32:33], v[28:29], off offset:512
	v_cvt_pk_bf16_f32 v28, v42, v43
	v_cvt_pk_bf16_f32 v29, v45, v44
	v_mul_f32_e32 v48, v68, v49
	v_mul_f32_e32 v49, v69, v51
	v_mul_f32_e32 v47, v70, v47
	v_mul_f32_e32 v46, v71, v46
	global_store_dwordx2 v[32:33], v[28:29], off offset:1024
	v_cvt_pk_bf16_f32 v28, v48, v49
	v_cvt_pk_bf16_f32 v29, v47, v46
	global_store_dwordx2 v[32:33], v[28:29], off offset:1536
	s_andn2_b64 exec, exec, s[20:21]
	s_nop 0
	v_lshl_add_u64 v[30:31], v[24:25], 0, v[20:21]
	v_add_co_u32_e32 v40, vcc, 0x3ec4a000, v30
	v_lshl_add_u64 v[28:29], v[22:23], 0, v[20:21]
	v_add_co_u32_e64 v32, s[4:5], s23, v30
	v_addc_co_u32_e32 v41, vcc, 0, v31, vcc
	s_nop 0
	v_addc_co_u32_e64 v33, s[4:5], 0, v31, s[4:5]
	v_add_co_u32_e32 v28, vcc, 0x42c4b000, v28
	s_waitcnt vmcnt(24)
	v_mov_b32_e32 v30, v208
	v_mov_b32_e32 v31, v209
	v_mov_b32_e32 v42, v210
	v_mov_b32_e32 v43, v211
	v_mov_b32_e32 v44, v212
	v_mov_b32_e32 v45, v213
	v_mov_b32_e32 v46, v214
	v_mov_b32_e32 v47, v215
	v_mov_b32_e32 v40, v216
	v_mov_b32_e32 v41, v217
	v_mov_b32_e32 v48, v218
	v_mov_b32_e32 v49, v219
	v_mov_b32_e32 v50, v220
	v_mov_b32_e32 v51, v221
	v_mov_b32_e32 v52, v222
	v_mov_b32_e32 v53, v223
	v_addc_co_u32_e32 v29, vcc, 0, v29, vcc
	v_add_u32_e32 v18, s14, v18
	v_cmp_lt_i32_e64 s[4:5], s24, v18
	s_or_b64 s[20:21], s[4:5], s[20:21]
	v_lshl_add_u64 v[22:23], v[22:23], 0, s[16:17]
	v_lshl_add_u64 v[24:25], v[24:25], 0, s[18:19]
	s_nop 0
	v_lshlrev_b32_e32 v28, 16, v30
	v_and_b32_e32 v29, 0xffff0000, v30
	s_nop 0
	v_lshlrev_b32_e32 v54, 16, v42
	v_and_b32_e32 v55, 0xffff0000, v42
	v_and_b32_e32 v30, 0xffff0000, v31
	v_lshlrev_b32_e32 v31, 16, v31
	v_and_b32_e32 v42, 0xffff0000, v43
	v_lshlrev_b32_e32 v43, 16, v43
	v_pk_mul_f32 v[60:61], v[28:29], v[28:29]
	v_pk_mul_f32 v[64:65], v[54:55], v[54:55]
	s_nop 0
	v_lshlrev_b32_e32 v19, 16, v40
	v_and_b32_e32 v39, 0xffff0000, v40
	v_lshlrev_b32_e32 v40, 16, v41
	v_and_b32_e32 v41, 0xffff0000, v41
	v_lshlrev_b32_e32 v56, 16, v44
	v_and_b32_e32 v57, 0xffff0000, v44
	v_lshlrev_b32_e32 v58, 16, v46
	v_and_b32_e32 v59, 0xffff0000, v46
	v_pk_mul_f32 v[62:63], v[30:31], v[30:31]
	v_pk_mul_f32 v[66:67], v[42:43], v[42:43]
	v_mul_f32_e32 v86, 0xbfb8aa3b, v40
	v_mul_f32_e32 v87, 0xbfb8aa3b, v41
	v_mov_b32_e32 v40, v64
	v_mov_b32_e32 v41, v60
	v_mov_b32_e32 v60, v65
	v_and_b32_e32 v44, 0xffff0000, v45
	v_lshlrev_b32_e32 v45, 16, v45
	v_and_b32_e32 v46, 0xffff0000, v47
	v_lshlrev_b32_e32 v47, 16, v47
	v_pk_mul_f32 v[68:69], v[56:57], v[56:57]
	v_pk_mul_f32 v[72:73], v[58:59], v[58:59]
	s_nop 0
	v_lshlrev_b32_e32 v76, 16, v48
	v_and_b32_e32 v77, 0xffff0000, v48
	v_lshlrev_b32_e32 v78, 16, v49
	v_and_b32_e32 v79, 0xffff0000, v49
	s_nop 0
	v_lshlrev_b32_e32 v80, 16, v50
	v_and_b32_e32 v50, 0xffff0000, v50
	v_lshlrev_b32_e32 v81, 16, v51
	v_and_b32_e32 v51, 0xffff0000, v51
	v_mov_b32_e32 v48, v67
	v_mov_b32_e32 v49, v63
	v_pk_add_f32 v[40:41], v[40:41], v[60:61]
	v_pk_mul_f32 v[70:71], v[44:45], v[44:45]
	v_pk_mul_f32 v[74:75], v[46:47], v[46:47]
	v_mov_b32_e32 v67, v62
	v_mul_f32_e32 v63, 0xbfb8aa3b, v77
	v_mul_f32_e32 v65, 0xbfb8aa3b, v79
	v_mul_f32_e32 v77, 0xbfb8aa3b, v50
	v_mul_f32_e32 v79, 0xbfb8aa3b, v51
	v_mov_b32_e32 v50, v72
	v_mov_b32_e32 v51, v68
	v_mov_b32_e32 v68, v73
	v_pk_add_f32 v[40:41], v[48:49], v[40:41]
	s_nop 0
	v_lshlrev_b32_e32 v82, 16, v52
	v_and_b32_e32 v83, 0xffff0000, v52
	v_lshlrev_b32_e32 v84, 16, v53
	v_and_b32_e32 v85, 0xffff0000, v53
	v_mov_b32_e32 v52, v75
	v_mov_b32_e32 v53, v71
	v_pk_add_f32 v[50:51], v[50:51], v[68:69]
	v_pk_add_f32 v[40:41], v[66:67], v[40:41]
	v_pk_add_f32 v[48:49], v[52:53], v[50:51]
	ds_bpermute_b32 v51, v1, v41
	ds_bpermute_b32 v50, v1, v40
	v_mov_b32_e32 v75, v70
	v_pk_add_f32 v[48:49], v[74:75], v[48:49]
	ds_bpermute_b32 v53, v1, v49
	ds_bpermute_b32 v52, v1, v48
	s_waitcnt lgkmcnt(2)
	v_pk_add_f32 v[40:41], v[40:41], v[50:51]
	ds_bpermute_b32 v51, v34, v41
	ds_bpermute_b32 v50, v34, v40
	v_mul_f32_e32 v19, 0xbfb8aa3b, v19
	s_waitcnt lgkmcnt(2)
	v_pk_add_f32 v[48:49], v[48:49], v[52:53]
	ds_bpermute_b32 v53, v34, v49
	ds_bpermute_b32 v52, v34, v48
	s_waitcnt lgkmcnt(2)
	v_pk_add_f32 v[40:41], v[40:41], v[50:51]
	ds_bpermute_b32 v51, v35, v41
	ds_bpermute_b32 v50, v35, v40
	v_mul_f32_e32 v39, 0xbfb8aa3b, v39
	s_waitcnt lgkmcnt(2)
	v_pk_add_f32 v[48:49], v[48:49], v[52:53]
	ds_bpermute_b32 v53, v35, v49
	ds_bpermute_b32 v52, v35, v48
	s_waitcnt lgkmcnt(2)
	v_pk_add_f32 v[40:41], v[40:41], v[50:51]
	ds_bpermute_b32 v51, v36, v41
	ds_bpermute_b32 v50, v36, v40
	v_mul_f32_e32 v62, 0xbfb8aa3b, v76
	s_waitcnt lgkmcnt(2)
	v_pk_add_f32 v[48:49], v[48:49], v[52:53]
	ds_bpermute_b32 v53, v36, v49
	ds_bpermute_b32 v52, v36, v48
	s_waitcnt lgkmcnt(2)
	v_pk_add_f32 v[40:41], v[40:41], v[50:51]
	ds_bpermute_b32 v51, v37, v41
	ds_bpermute_b32 v50, v37, v40
	v_mul_f32_e32 v76, 0xbfb8aa3b, v80
	s_waitcnt lgkmcnt(2)
	v_pk_add_f32 v[48:49], v[48:49], v[52:53]
	ds_bpermute_b32 v53, v37, v49
	ds_bpermute_b32 v52, v37, v48
	s_waitcnt lgkmcnt(2)
	v_pk_add_f32 v[40:41], v[40:41], v[50:51]
	ds_bpermute_b32 v51, v38, v41
	ds_bpermute_b32 v50, v38, v40
	v_exp_f32_e32 v19, v19
	s_waitcnt lgkmcnt(2)
	v_pk_add_f32 v[48:49], v[48:49], v[52:53]
	ds_bpermute_b32 v53, v38, v49
	ds_bpermute_b32 v52, v38, v48
	s_waitcnt lgkmcnt(2)
	v_pk_add_f32 v[40:41], v[40:41], v[50:51]
	v_exp_f32_e32 v39, v39
	v_pk_fma_f32 v[40:41], v[40:41], s[22:23], v[26:27] op_sel_hi:[1,0,0]
	v_exp_f32_e32 v80, v86
	v_mul_f32_e32 v50, 0x4b800000, v41
	v_cmp_gt_f32_e64 s[8:9], s15, v41
	s_waitcnt lgkmcnt(0)
	v_pk_add_f32 v[48:49], v[48:49], v[52:53]
	v_mul_f32_e32 v64, 0xbfb8aa3b, v78
	v_cndmask_b32_e64 v41, v41, v50, s[8:9]
	v_mul_f32_e32 v78, 0xbfb8aa3b, v81
	v_exp_f32_e32 v81, v87
	v_pk_fma_f32 v[48:49], v[48:49], s[22:23], v[26:27] op_sel_hi:[1,0,0]
	v_mul_f32_e32 v51, 0x4b800000, v40
	v_cmp_gt_f32_e32 vcc, s15, v40
	v_rsq_f32_e32 v41, v41
	v_exp_f32_e32 v60, v62
	v_exp_f32_e32 v61, v63
	v_exp_f32_e32 v62, v64
	v_exp_f32_e32 v63, v65
	v_mul_f32_e32 v52, 0x4b800000, v49
	v_mul_f32_e32 v53, 0x4b800000, v48
	v_cmp_gt_f32_e64 s[4:5], s15, v48
	v_cmp_gt_f32_e64 s[6:7], s15, v49
	v_cndmask_b32_e32 v40, v40, v51, vcc
	v_mul_f32_e32 v70, 0xbfb8aa3b, v82
	v_mul_f32_e32 v71, 0xbfb8aa3b, v83
	v_mul_f32_e32 v72, 0xbfb8aa3b, v84
	v_mul_f32_e32 v73, 0xbfb8aa3b, v85
	v_exp_f32_e32 v64, v76
	v_exp_f32_e32 v65, v77
	v_exp_f32_e32 v76, v78
	v_exp_f32_e32 v77, v79
	v_cndmask_b32_e64 v49, v49, v52, s[6:7]
	v_cndmask_b32_e64 v48, v48, v53, s[4:5]
	v_rsq_f32_e32 v40, v40
	v_exp_f32_e32 v68, v70
	v_exp_f32_e32 v69, v71
	v_exp_f32_e32 v70, v72
	v_exp_f32_e32 v71, v73
	v_add_f32_e32 v19, 1.0, v19
	v_add_f32_e32 v39, 1.0, v39
	v_add_f32_e32 v66, 1.0, v80
	v_rsq_f32_e32 v49, v49
	v_rsq_f32_e32 v48, v48
	v_add_f32_e32 v67, 1.0, v81
	v_rcp_f32_e32 v19, v19
	v_rcp_f32_e32 v39, v39
	v_rcp_f32_e32 v66, v66
	v_mul_f32_e32 v50, 0x45800000, v41
	v_add_f32_e32 v60, 1.0, v60
	v_add_f32_e32 v61, 1.0, v61
	v_add_f32_e32 v62, 1.0, v62
	v_add_f32_e32 v63, 1.0, v63
	v_rcp_f32_e32 v67, v67
	v_cndmask_b32_e64 v41, v41, v50, s[8:9]
	v_add_f32_e32 v64, 1.0, v64
	v_add_f32_e32 v65, 1.0, v65
	v_add_f32_e32 v72, 1.0, v76
	v_add_f32_e32 v73, 1.0, v77
	v_rcp_f32_e32 v60, v60
	v_rcp_f32_e32 v61, v61
	v_rcp_f32_e32 v62, v62
	v_rcp_f32_e32 v63, v63
	v_mul_f32_e32 v51, 0x45800000, v40
	v_mul_f32_e32 v28, v41, v28
	v_mul_f32_e32 v29, v41, v29
	v_mul_f32_e32 v31, v41, v31
	v_add_f32_e32 v68, 1.0, v68
	v_add_f32_e32 v69, 1.0, v69
	v_add_f32_e32 v70, 1.0, v70
	v_add_f32_e32 v71, 1.0, v71
	v_rcp_f32_e32 v64, v64
	v_rcp_f32_e32 v65, v65
	v_rcp_f32_e32 v72, v72
	v_rcp_f32_e32 v73, v73
	v_mul_f32_e32 v52, 0x45800000, v49
	v_mul_f32_e32 v53, 0x45800000, v48
	v_cndmask_b32_e32 v40, v40, v51, vcc
	v_mul_f32_e32 v30, v41, v30
	v_mul_f32_e32 v28, v14, v28
	v_mul_f32_e32 v29, v15, v29
	v_mul_f32_e32 v31, v16, v31
	v_rcp_f32_e32 v68, v68
	v_rcp_f32_e32 v69, v69
	v_rcp_f32_e32 v70, v70
	v_rcp_f32_e32 v71, v71
	v_cndmask_b32_e64 v49, v49, v52, s[6:7]
	v_cndmask_b32_e64 v48, v48, v53, s[4:5]
	v_mul_f32_e32 v41, v40, v54
	v_mul_f32_e32 v50, v40, v55
	v_mul_f32_e32 v43, v40, v43
	v_mul_f32_e32 v40, v40, v42
	v_mul_f32_e32 v30, v17, v30
	v_mul_f32_e32 v19, v19, v28
	v_mul_f32_e32 v28, v39, v29
	v_mul_f32_e32 v29, v66, v31
	v_mul_f32_e32 v42, v49, v56
	v_mul_f32_e32 v51, v49, v57
	v_mul_f32_e32 v45, v49, v45
	v_mul_f32_e32 v44, v49, v44
	v_mul_f32_e32 v49, v48, v58
	v_mul_f32_e32 v52, v48, v59
	v_mul_f32_e32 v47, v48, v47
	v_mul_f32_e32 v46, v48, v46
	v_mul_f32_e32 v41, v10, v41
	v_mul_f32_e32 v48, v11, v50
	v_mul_f32_e32 v43, v12, v43
	v_mul_f32_e32 v40, v13, v40
	v_mul_f32_e32 v30, v67, v30
	v_cvt_pk_bf16_f32 v28, v19, v28
	v_cvt_pk_bf16_f32 v29, v29, v30
	v_mul_f32_e32 v42, v6, v42
	v_mul_f32_e32 v50, v7, v51
	v_mul_f32_e32 v45, v8, v45
	v_mul_f32_e32 v44, v9, v44
	v_mul_f32_e32 v31, v60, v41
	v_mul_f32_e32 v39, v61, v48
	v_mul_f32_e32 v41, v62, v43
	v_mul_f32_e32 v40, v63, v40
	global_store_dwordx2 v[32:33], v[28:29], off
	v_cvt_pk_bf16_f32 v28, v31, v39
	v_cvt_pk_bf16_f32 v29, v41, v40
	v_mul_f32_e32 v49, v2, v49
	v_mul_f32_e32 v51, v3, v52
	v_mul_f32_e32 v47, v4, v47
	v_mul_f32_e32 v46, v5, v46
	v_mul_f32_e32 v42, v64, v42
	v_mul_f32_e32 v43, v65, v50
	v_mul_f32_e32 v45, v72, v45
	v_mul_f32_e32 v44, v73, v44
	global_store_dwordx2 v[32:33], v[28:29], off offset:512
	v_cvt_pk_bf16_f32 v28, v42, v43
	v_cvt_pk_bf16_f32 v29, v45, v44
	v_mul_f32_e32 v48, v68, v49
	v_mul_f32_e32 v49, v69, v51
	v_mul_f32_e32 v47, v70, v47
	v_mul_f32_e32 v46, v71, v46
	global_store_dwordx2 v[32:33], v[28:29], off offset:1024
	v_cvt_pk_bf16_f32 v28, v48, v49
	v_cvt_pk_bf16_f32 v29, v47, v46
	global_store_dwordx2 v[32:33], v[28:29], off offset:1536
	s_andn2_b64 exec, exec, s[20:21]
